# layer-1 w_in bf16 transpose moved from the up-front convert phase into layer-0 converter workgroups slack; peeled first K-trip (no accumulator zeroing)
# speedup vs baseline: 1.0063x; 1.0050x over previous
.LBB0_45:
	s_waitcnt lgkmcnt(0)
	s_barrier
	v_readlane_b32 s20, v255, 60
	s_nop 3
	s_cmp_lg_u32 s20, 0
	s_cbranch_scc1 .Lwin1_done
	s_load_dwordx2 s[12:13], s[8:9], 0x10
	v_readlane_b32 s3, v254, 12
	v_lshrrev_b32_e32 v19, 3, v67
	v_and_b32_e32 v28, 7, v67
	v_lshlrev_b32_e32 v29, 4, v28
	v_mul_u32_u24_e32 v6, 0x5e000, v19
	v_add_u32_e32 v6, v6, v29
	v_add_u32_e32 v7, 0xbc00, v6
	v_add_u32_e32 v8, 0x17800, v6
	v_add_u32_e32 v9, 0x23400, v6
	v_add_u32_e32 v10, 0x2f000, v6
	v_add_u32_e32 v11, 0x3ac00, v6
	v_add_u32_e32 v12, 0x46800, v6
	v_add_u32_e32 v13, 0x52400, v6
	v_lshlrev_b32_e32 v29, 4, v19
	v_lshl_add_u32 v14, v28, 14, v29
	v_add_u32_e32 v15, 0x1000, v14
	v_add_u32_e32 v16, 0x2000, v14
	v_add_u32_e32 v17, 0x3000, v14
	s_add_i32 s3, s50, s3
	s_cmp_ge_u32 s3, 0x178
	s_cselect_b32 s17, 1, 0
	s_cselect_b32 s20, 0x178, 0
	s_sub_i32 s16, s3, s20
	s_mov_b32 s18, s16
	s_mov_b32 s19, s17
	s_waitcnt lgkmcnt(0)
	s_add_u32 s12, s12, 0x5e00000
	s_addc_u32 s13, s13, 0
	s_add_u32 s14, s10, 0x3100000
	s_addc_u32 s15, s11, 0
	s_mul_i32 s20, s17, 0x2f0000
	s_lshl_b32 s21, s16, 7
	s_add_u32 s24, s12, s20
	s_addc_u32 s25, s13, 0
	s_add_u32 s24, s24, s21
	s_addc_u32 s25, s25, 0
	global_load_dwordx4 v[32:35], v6, s[24:25] nt
	global_load_dwordx4 v[36:39], v7, s[24:25] nt
	global_load_dwordx4 v[40:43], v8, s[24:25] nt
	global_load_dwordx4 v[44:47], v9, s[24:25] nt
	global_load_dwordx4 v[48:51], v10, s[24:25] nt
	global_load_dwordx4 v[52:55], v11, s[24:25] nt
	global_load_dwordx4 v[56:59], v12, s[24:25] nt
	global_load_dwordx4 v[60:63], v13, s[24:25] nt
	s_add_i32 s16, s16, 0x88
	s_add_i32 s17, s17, 1
	s_cmp_ge_u32 s16, 0x178
	s_cselect_b32 s20, 0x178, 0
	s_cselect_b32 s21, 1, 0
	s_sub_i32 s16, s16, s20
	s_add_i32 s17, s17, s21
	s_cmp_ge_u32 s17, 32
	s_cselect_b32 s20, 32, 0
	s_sub_i32 s17, s17, s20
	s_mul_i32 s20, s17, 0x2f0000
	s_lshl_b32 s21, s16, 7
	s_add_u32 s24, s12, s20
	s_addc_u32 s25, s13, 0
	s_add_u32 s24, s24, s21
	s_addc_u32 s25, s25, 0
	global_load_dwordx4 v[64:67], v6, s[24:25] nt
	global_load_dwordx4 v[68:71], v7, s[24:25] nt
	global_load_dwordx4 v[72:75], v8, s[24:25] nt
	global_load_dwordx4 v[76:79], v9, s[24:25] nt
	global_load_dwordx4 v[80:83], v10, s[24:25] nt
	global_load_dwordx4 v[84:87], v11, s[24:25] nt
	global_load_dwordx4 v[88:91], v12, s[24:25] nt
	global_load_dwordx4 v[92:95], v13, s[24:25] nt
	s_add_i32 s16, s16, 0x88
	s_add_i32 s17, s17, 1
	s_cmp_ge_u32 s16, 0x178
	s_cselect_b32 s20, 0x178, 0
	s_cselect_b32 s21, 1, 0
	s_sub_i32 s16, s16, s20
	s_add_i32 s17, s17, s21
	s_cmp_ge_u32 s17, 32
	s_cselect_b32 s20, 32, 0
	s_sub_i32 s17, s17, s20
	s_mul_i32 s20, s17, 0x2f0000
	s_lshl_b32 s21, s16, 7
	s_add_u32 s24, s12, s20
	s_addc_u32 s25, s13, 0
	s_add_u32 s24, s24, s21
	s_addc_u32 s25, s25, 0
	global_load_dwordx4 v[96:99], v6, s[24:25] nt
	global_load_dwordx4 v[100:103], v7, s[24:25] nt
	global_load_dwordx4 v[104:107], v8, s[24:25] nt
	global_load_dwordx4 v[108:111], v9, s[24:25] nt
	global_load_dwordx4 v[112:115], v10, s[24:25] nt
	global_load_dwordx4 v[116:119], v11, s[24:25] nt
	global_load_dwordx4 v[120:123], v12, s[24:25] nt
	global_load_dwordx4 v[124:127], v13, s[24:25] nt
	s_add_i32 s16, s16, 0x88
	s_add_i32 s17, s17, 1
	s_cmp_ge_u32 s16, 0x178
	s_cselect_b32 s20, 0x178, 0
	s_cselect_b32 s21, 1, 0
	s_sub_i32 s16, s16, s20
	s_add_i32 s17, s17, s21
	s_cmp_ge_u32 s17, 32
	s_cselect_b32 s20, 32, 0
	s_sub_i32 s17, s17, s20
	s_waitcnt vmcnt(16)
	s_lshl_b32 s20, s18, 17
	s_lshl_b32 s21, s19, 7
	s_add_u32 s26, s14, s20
	s_addc_u32 s27, s15, 0
	s_add_u32 s26, s26, s21
	s_addc_u32 s27, s27, 0
	v_cvt_pk_bf16_f32 v20, v32, v36
	v_cvt_pk_bf16_f32 v21, v40, v44
	v_cvt_pk_bf16_f32 v22, v48, v52
	v_cvt_pk_bf16_f32 v23, v56, v60
	global_store_dwordx4 v14, v[20:23], s[26:27]
	v_cvt_pk_bf16_f32 v24, v33, v37
	v_cvt_pk_bf16_f32 v25, v41, v45
	v_cvt_pk_bf16_f32 v26, v49, v53
	v_cvt_pk_bf16_f32 v27, v57, v61
	global_store_dwordx4 v15, v[24:27], s[26:27]
	v_cvt_pk_bf16_f32 v20, v34, v38
	v_cvt_pk_bf16_f32 v21, v42, v46
	v_cvt_pk_bf16_f32 v22, v50, v54
	v_cvt_pk_bf16_f32 v23, v58, v62
	global_store_dwordx4 v16, v[20:23], s[26:27]
	v_cvt_pk_bf16_f32 v24, v35, v39
	v_cvt_pk_bf16_f32 v25, v43, v47
	v_cvt_pk_bf16_f32 v26, v51, v55
	v_cvt_pk_bf16_f32 v27, v59, v63
	global_store_dwordx4 v17, v[24:27], s[26:27]
	s_add_i32 s18, s18, 0x88
	s_add_i32 s19, s19, 1
	s_cmp_ge_u32 s18, 0x178
	s_cselect_b32 s20, 0x178, 0
	s_cselect_b32 s21, 1, 0
	s_sub_i32 s18, s18, s20
	s_add_i32 s19, s19, s21
	s_cmp_ge_u32 s19, 32
	s_cselect_b32 s20, 32, 0
	s_sub_i32 s19, s19, s20
	s_mul_i32 s20, s17, 0x2f0000
	s_lshl_b32 s21, s16, 7
	s_add_u32 s24, s12, s20
	s_addc_u32 s25, s13, 0
	s_add_u32 s24, s24, s21
	s_addc_u32 s25, s25, 0
	global_load_dwordx4 v[32:35], v6, s[24:25] nt
	global_load_dwordx4 v[36:39], v7, s[24:25] nt
	global_load_dwordx4 v[40:43], v8, s[24:25] nt
	global_load_dwordx4 v[44:47], v9, s[24:25] nt
	global_load_dwordx4 v[48:51], v10, s[24:25] nt
	global_load_dwordx4 v[52:55], v11, s[24:25] nt
	global_load_dwordx4 v[56:59], v12, s[24:25] nt
	global_load_dwordx4 v[60:63], v13, s[24:25] nt
	s_add_i32 s16, s16, 0x88
	s_add_i32 s17, s17, 1
	s_cmp_ge_u32 s16, 0x178
	s_cselect_b32 s20, 0x178, 0
	s_cselect_b32 s21, 1, 0
	s_sub_i32 s16, s16, s20
	s_add_i32 s17, s17, s21
	s_cmp_ge_u32 s17, 32
	s_cselect_b32 s20, 32, 0
	s_sub_i32 s17, s17, s20
	s_waitcnt vmcnt(20)
	s_lshl_b32 s20, s18, 17
	s_lshl_b32 s21, s19, 7
	s_add_u32 s26, s14, s20
	s_addc_u32 s27, s15, 0
	s_add_u32 s26, s26, s21
	s_addc_u32 s27, s27, 0
	v_cvt_pk_bf16_f32 v20, v64, v68
	v_cvt_pk_bf16_f32 v21, v72, v76
	v_cvt_pk_bf16_f32 v22, v80, v84
	v_cvt_pk_bf16_f32 v23, v88, v92
	global_store_dwordx4 v14, v[20:23], s[26:27]
	v_cvt_pk_bf16_f32 v24, v65, v69
	v_cvt_pk_bf16_f32 v25, v73, v77
	v_cvt_pk_bf16_f32 v26, v81, v85
	v_cvt_pk_bf16_f32 v27, v89, v93
	global_store_dwordx4 v15, v[24:27], s[26:27]
	v_cvt_pk_bf16_f32 v20, v66, v70
	v_cvt_pk_bf16_f32 v21, v74, v78
	v_cvt_pk_bf16_f32 v22, v82, v86
	v_cvt_pk_bf16_f32 v23, v90, v94
	global_store_dwordx4 v16, v[20:23], s[26:27]
	v_cvt_pk_bf16_f32 v24, v67, v71
	v_cvt_pk_bf16_f32 v25, v75, v79
	v_cvt_pk_bf16_f32 v26, v83, v87
	v_cvt_pk_bf16_f32 v27, v91, v95
	global_store_dwordx4 v17, v[24:27], s[26:27]
	s_add_i32 s18, s18, 0x88
	s_add_i32 s19, s19, 1
	s_cmp_ge_u32 s18, 0x178
	s_cselect_b32 s20, 0x178, 0
	s_cselect_b32 s21, 1, 0
	s_sub_i32 s18, s18, s20
	s_add_i32 s19, s19, s21
	s_cmp_ge_u32 s19, 32
	s_cselect_b32 s20, 32, 0
	s_sub_i32 s19, s19, s20
	s_mul_i32 s20, s17, 0x2f0000
	s_lshl_b32 s21, s16, 7
	s_add_u32 s24, s12, s20
	s_addc_u32 s25, s13, 0
	s_add_u32 s24, s24, s21
	s_addc_u32 s25, s25, 0
	global_load_dwordx4 v[64:67], v6, s[24:25] nt
	global_load_dwordx4 v[68:71], v7, s[24:25] nt
	global_load_dwordx4 v[72:75], v8, s[24:25] nt
	global_load_dwordx4 v[76:79], v9, s[24:25] nt
	global_load_dwordx4 v[80:83], v10, s[24:25] nt
	global_load_dwordx4 v[84:87], v11, s[24:25] nt
	global_load_dwordx4 v[88:91], v12, s[24:25] nt
	global_load_dwordx4 v[92:95], v13, s[24:25] nt
	s_add_i32 s16, s16, 0x88
	s_add_i32 s17, s17, 1
	s_cmp_ge_u32 s16, 0x178
	s_cselect_b32 s20, 0x178, 0
	s_cselect_b32 s21, 1, 0
	s_sub_i32 s16, s16, s20
	s_add_i32 s17, s17, s21
	s_cmp_ge_u32 s17, 32
	s_cselect_b32 s20, 32, 0
	s_sub_i32 s17, s17, s20
	s_waitcnt vmcnt(24)
	s_lshl_b32 s20, s18, 17
	s_lshl_b32 s21, s19, 7
	s_add_u32 s26, s14, s20
	s_addc_u32 s27, s15, 0
	s_add_u32 s26, s26, s21
	s_addc_u32 s27, s27, 0
	v_cvt_pk_bf16_f32 v20, v96, v100
	v_cvt_pk_bf16_f32 v21, v104, v108
	v_cvt_pk_bf16_f32 v22, v112, v116
	v_cvt_pk_bf16_f32 v23, v120, v124
	global_store_dwordx4 v14, v[20:23], s[26:27]
	v_cvt_pk_bf16_f32 v24, v97, v101
	v_cvt_pk_bf16_f32 v25, v105, v109
	v_cvt_pk_bf16_f32 v26, v113, v117
	v_cvt_pk_bf16_f32 v27, v121, v125
	global_store_dwordx4 v15, v[24:27], s[26:27]
	v_cvt_pk_bf16_f32 v20, v98, v102
	v_cvt_pk_bf16_f32 v21, v106, v110
	v_cvt_pk_bf16_f32 v22, v114, v118
	v_cvt_pk_bf16_f32 v23, v122, v126
	global_store_dwordx4 v16, v[20:23], s[26:27]
	v_cvt_pk_bf16_f32 v24, v99, v103
	v_cvt_pk_bf16_f32 v25, v107, v111
	v_cvt_pk_bf16_f32 v26, v115, v119
	v_cvt_pk_bf16_f32 v27, v123, v127
	global_store_dwordx4 v17, v[24:27], s[26:27]
	s_add_i32 s18, s18, 0x88
	s_add_i32 s19, s19, 1
	s_cmp_ge_u32 s18, 0x178
	s_cselect_b32 s20, 0x178, 0
	s_cselect_b32 s21, 1, 0
	s_sub_i32 s18, s18, s20
	s_add_i32 s19, s19, s21
	s_cmp_ge_u32 s19, 32
	s_cselect_b32 s20, 32, 0
	s_sub_i32 s19, s19, s20
	s_mul_i32 s20, s17, 0x2f0000
	s_lshl_b32 s21, s16, 7
	s_add_u32 s24, s12, s20
	s_addc_u32 s25, s13, 0
	s_add_u32 s24, s24, s21
	s_addc_u32 s25, s25, 0
	global_load_dwordx4 v[96:99], v6, s[24:25] nt
	global_load_dwordx4 v[100:103], v7, s[24:25] nt
	global_load_dwordx4 v[104:107], v8, s[24:25] nt
	global_load_dwordx4 v[108:111], v9, s[24:25] nt
	global_load_dwordx4 v[112:115], v10, s[24:25] nt
	global_load_dwordx4 v[116:119], v11, s[24:25] nt
	global_load_dwordx4 v[120:123], v12, s[24:25] nt
	global_load_dwordx4 v[124:127], v13, s[24:25] nt
	s_add_i32 s16, s16, 0x88
	s_add_i32 s17, s17, 1
	s_cmp_ge_u32 s16, 0x178
	s_cselect_b32 s20, 0x178, 0
	s_cselect_b32 s21, 1, 0
	s_sub_i32 s16, s16, s20
	s_add_i32 s17, s17, s21
	s_cmp_ge_u32 s17, 32
	s_cselect_b32 s20, 32, 0
	s_sub_i32 s17, s17, s20
	s_waitcnt vmcnt(24)
	s_lshl_b32 s20, s18, 17
	s_lshl_b32 s21, s19, 7
	s_add_u32 s26, s14, s20
	s_addc_u32 s27, s15, 0
	s_add_u32 s26, s26, s21
	s_addc_u32 s27, s27, 0
	v_cvt_pk_bf16_f32 v20, v32, v36
	v_cvt_pk_bf16_f32 v21, v40, v44
	v_cvt_pk_bf16_f32 v22, v48, v52
	v_cvt_pk_bf16_f32 v23, v56, v60
	global_store_dwordx4 v14, v[20:23], s[26:27]
	v_cvt_pk_bf16_f32 v24, v33, v37
	v_cvt_pk_bf16_f32 v25, v41, v45
	v_cvt_pk_bf16_f32 v26, v49, v53
	v_cvt_pk_bf16_f32 v27, v57, v61
	global_store_dwordx4 v15, v[24:27], s[26:27]
	v_cvt_pk_bf16_f32 v20, v34, v38
	v_cvt_pk_bf16_f32 v21, v42, v46
	v_cvt_pk_bf16_f32 v22, v50, v54
	v_cvt_pk_bf16_f32 v23, v58, v62
	global_store_dwordx4 v16, v[20:23], s[26:27]
	v_cvt_pk_bf16_f32 v24, v35, v39
	v_cvt_pk_bf16_f32 v25, v43, v47
	v_cvt_pk_bf16_f32 v26, v51, v55
	v_cvt_pk_bf16_f32 v27, v59, v63
	global_store_dwordx4 v17, v[24:27], s[26:27]
	s_add_i32 s18, s18, 0x88
	s_add_i32 s19, s19, 1
	s_cmp_ge_u32 s18, 0x178
	s_cselect_b32 s20, 0x178, 0
	s_cselect_b32 s21, 1, 0
	s_sub_i32 s18, s18, s20
	s_add_i32 s19, s19, s21
	s_cmp_ge_u32 s19, 32
	s_cselect_b32 s20, 32, 0
	s_sub_i32 s19, s19, s20
	s_mul_i32 s20, s17, 0x2f0000
	s_lshl_b32 s21, s16, 7
	s_add_u32 s24, s12, s20
	s_addc_u32 s25, s13, 0
	s_add_u32 s24, s24, s21
	s_addc_u32 s25, s25, 0
	global_load_dwordx4 v[32:35], v6, s[24:25] nt
	global_load_dwordx4 v[36:39], v7, s[24:25] nt
	global_load_dwordx4 v[40:43], v8, s[24:25] nt
	global_load_dwordx4 v[44:47], v9, s[24:25] nt
	global_load_dwordx4 v[48:51], v10, s[24:25] nt
	global_load_dwordx4 v[52:55], v11, s[24:25] nt
	global_load_dwordx4 v[56:59], v12, s[24:25] nt
	global_load_dwordx4 v[60:63], v13, s[24:25] nt
	s_add_i32 s16, s16, 0x88
	s_add_i32 s17, s17, 1
	s_cmp_ge_u32 s16, 0x178
	s_cselect_b32 s20, 0x178, 0
	s_cselect_b32 s21, 1, 0
	s_sub_i32 s16, s16, s20
	s_add_i32 s17, s17, s21
	s_cmp_ge_u32 s17, 32
	s_cselect_b32 s20, 32, 0
	s_sub_i32 s17, s17, s20
	s_waitcnt vmcnt(24)
	s_lshl_b32 s20, s18, 17
	s_lshl_b32 s21, s19, 7
	s_add_u32 s26, s14, s20
	s_addc_u32 s27, s15, 0
	s_add_u32 s26, s26, s21
	s_addc_u32 s27, s27, 0
	v_cvt_pk_bf16_f32 v20, v64, v68
	v_cvt_pk_bf16_f32 v21, v72, v76
	v_cvt_pk_bf16_f32 v22, v80, v84
	v_cvt_pk_bf16_f32 v23, v88, v92
	global_store_dwordx4 v14, v[20:23], s[26:27]
	v_cvt_pk_bf16_f32 v24, v65, v69
	v_cvt_pk_bf16_f32 v25, v73, v77
	v_cvt_pk_bf16_f32 v26, v81, v85
	v_cvt_pk_bf16_f32 v27, v89, v93
	global_store_dwordx4 v15, v[24:27], s[26:27]
	v_cvt_pk_bf16_f32 v20, v66, v70
	v_cvt_pk_bf16_f32 v21, v74, v78
	v_cvt_pk_bf16_f32 v22, v82, v86
	v_cvt_pk_bf16_f32 v23, v90, v94
	global_store_dwordx4 v16, v[20:23], s[26:27]
	v_cvt_pk_bf16_f32 v24, v67, v71
	v_cvt_pk_bf16_f32 v25, v75, v79
	v_cvt_pk_bf16_f32 v26, v83, v87
	v_cvt_pk_bf16_f32 v27, v91, v95
	global_store_dwordx4 v17, v[24:27], s[26:27]
	s_add_i32 s18, s18, 0x88
	s_add_i32 s19, s19, 1
	s_cmp_ge_u32 s18, 0x178
	s_cselect_b32 s20, 0x178, 0
	s_cselect_b32 s21, 1, 0
	s_sub_i32 s18, s18, s20
	s_add_i32 s19, s19, s21
	s_cmp_ge_u32 s19, 32
	s_cselect_b32 s20, 32, 0
	s_sub_i32 s19, s19, s20
	s_mul_i32 s20, s17, 0x2f0000
	s_lshl_b32 s21, s16, 7
	s_add_u32 s24, s12, s20
	s_addc_u32 s25, s13, 0
	s_add_u32 s24, s24, s21
	s_addc_u32 s25, s25, 0
	global_load_dwordx4 v[64:67], v6, s[24:25] nt
	global_load_dwordx4 v[68:71], v7, s[24:25] nt
	global_load_dwordx4 v[72:75], v8, s[24:25] nt
	global_load_dwordx4 v[76:79], v9, s[24:25] nt
	global_load_dwordx4 v[80:83], v10, s[24:25] nt
	global_load_dwordx4 v[84:87], v11, s[24:25] nt
	global_load_dwordx4 v[88:91], v12, s[24:25] nt
	global_load_dwordx4 v[92:95], v13, s[24:25] nt
	s_add_i32 s16, s16, 0x88
	s_add_i32 s17, s17, 1
	s_cmp_ge_u32 s16, 0x178
	s_cselect_b32 s20, 0x178, 0
	s_cselect_b32 s21, 1, 0
	s_sub_i32 s16, s16, s20
	s_add_i32 s17, s17, s21
	s_cmp_ge_u32 s17, 32
	s_cselect_b32 s20, 32, 0
	s_sub_i32 s17, s17, s20
	s_waitcnt vmcnt(24)
	s_lshl_b32 s20, s18, 17
	s_lshl_b32 s21, s19, 7
	s_add_u32 s26, s14, s20
	s_addc_u32 s27, s15, 0
	s_add_u32 s26, s26, s21
	s_addc_u32 s27, s27, 0
	v_cvt_pk_bf16_f32 v20, v96, v100
	v_cvt_pk_bf16_f32 v21, v104, v108
	v_cvt_pk_bf16_f32 v22, v112, v116
	v_cvt_pk_bf16_f32 v23, v120, v124
	global_store_dwordx4 v14, v[20:23], s[26:27]
	v_cvt_pk_bf16_f32 v24, v97, v101
	v_cvt_pk_bf16_f32 v25, v105, v109
	v_cvt_pk_bf16_f32 v26, v113, v117
	v_cvt_pk_bf16_f32 v27, v121, v125
	global_store_dwordx4 v15, v[24:27], s[26:27]
	v_cvt_pk_bf16_f32 v20, v98, v102
	v_cvt_pk_bf16_f32 v21, v106, v110
	v_cvt_pk_bf16_f32 v22, v114, v118
	v_cvt_pk_bf16_f32 v23, v122, v126
	global_store_dwordx4 v16, v[20:23], s[26:27]
	v_cvt_pk_bf16_f32 v24, v99, v103
	v_cvt_pk_bf16_f32 v25, v107, v111
	v_cvt_pk_bf16_f32 v26, v115, v119
	v_cvt_pk_bf16_f32 v27, v123, v127
	global_store_dwordx4 v17, v[24:27], s[26:27]
	s_add_i32 s18, s18, 0x88
	s_add_i32 s19, s19, 1
	s_cmp_ge_u32 s18, 0x178
	s_cselect_b32 s20, 0x178, 0
	s_cselect_b32 s21, 1, 0
	s_sub_i32 s18, s18, s20
	s_add_i32 s19, s19, s21
	s_cmp_ge_u32 s19, 32
	s_cselect_b32 s20, 32, 0
	s_sub_i32 s19, s19, s20
	s_mul_i32 s20, s17, 0x2f0000
	s_lshl_b32 s21, s16, 7
	s_add_u32 s24, s12, s20
	s_addc_u32 s25, s13, 0
	s_add_u32 s24, s24, s21
	s_addc_u32 s25, s25, 0
	global_load_dwordx4 v[96:99], v6, s[24:25] nt
	global_load_dwordx4 v[100:103], v7, s[24:25] nt
	global_load_dwordx4 v[104:107], v8, s[24:25] nt
	global_load_dwordx4 v[108:111], v9, s[24:25] nt
	global_load_dwordx4 v[112:115], v10, s[24:25] nt
	global_load_dwordx4 v[116:119], v11, s[24:25] nt
	global_load_dwordx4 v[120:123], v12, s[24:25] nt
	global_load_dwordx4 v[124:127], v13, s[24:25] nt
	s_add_i32 s16, s16, 0x88
	s_add_i32 s17, s17, 1
	s_cmp_ge_u32 s16, 0x178
	s_cselect_b32 s20, 0x178, 0
	s_cselect_b32 s21, 1, 0
	s_sub_i32 s16, s16, s20
	s_add_i32 s17, s17, s21
	s_cmp_ge_u32 s17, 32
	s_cselect_b32 s20, 32, 0
	s_sub_i32 s17, s17, s20
	s_waitcnt vmcnt(24)
	s_lshl_b32 s20, s18, 17
	s_lshl_b32 s21, s19, 7
	s_add_u32 s26, s14, s20
	s_addc_u32 s27, s15, 0
	s_add_u32 s26, s26, s21
	s_addc_u32 s27, s27, 0
	v_cvt_pk_bf16_f32 v20, v32, v36
	v_cvt_pk_bf16_f32 v21, v40, v44
	v_cvt_pk_bf16_f32 v22, v48, v52
	v_cvt_pk_bf16_f32 v23, v56, v60
	global_store_dwordx4 v14, v[20:23], s[26:27]
	v_cvt_pk_bf16_f32 v24, v33, v37
	v_cvt_pk_bf16_f32 v25, v41, v45
	v_cvt_pk_bf16_f32 v26, v49, v53
	v_cvt_pk_bf16_f32 v27, v57, v61
	global_store_dwordx4 v15, v[24:27], s[26:27]
	v_cvt_pk_bf16_f32 v20, v34, v38
	v_cvt_pk_bf16_f32 v21, v42, v46
	v_cvt_pk_bf16_f32 v22, v50, v54
	v_cvt_pk_bf16_f32 v23, v58, v62
	global_store_dwordx4 v16, v[20:23], s[26:27]
	v_cvt_pk_bf16_f32 v24, v35, v39
	v_cvt_pk_bf16_f32 v25, v43, v47
	v_cvt_pk_bf16_f32 v26, v51, v55
	v_cvt_pk_bf16_f32 v27, v59, v63
	global_store_dwordx4 v17, v[24:27], s[26:27]
	s_add_i32 s18, s18, 0x88
	s_add_i32 s19, s19, 1
	s_cmp_ge_u32 s18, 0x178
	s_cselect_b32 s20, 0x178, 0
	s_cselect_b32 s21, 1, 0
	s_sub_i32 s18, s18, s20
	s_add_i32 s19, s19, s21
	s_cmp_ge_u32 s19, 32
	s_cselect_b32 s20, 32, 0
	s_sub_i32 s19, s19, s20
	s_mul_i32 s20, s17, 0x2f0000
	s_lshl_b32 s21, s16, 7
	s_add_u32 s24, s12, s20
	s_addc_u32 s25, s13, 0
	s_add_u32 s24, s24, s21
	s_addc_u32 s25, s25, 0
	global_load_dwordx4 v[32:35], v6, s[24:25] nt
	global_load_dwordx4 v[36:39], v7, s[24:25] nt
	global_load_dwordx4 v[40:43], v8, s[24:25] nt
	global_load_dwordx4 v[44:47], v9, s[24:25] nt
	global_load_dwordx4 v[48:51], v10, s[24:25] nt
	global_load_dwordx4 v[52:55], v11, s[24:25] nt
	global_load_dwordx4 v[56:59], v12, s[24:25] nt
	global_load_dwordx4 v[60:63], v13, s[24:25] nt
	s_add_i32 s16, s16, 0x88
	s_add_i32 s17, s17, 1
	s_cmp_ge_u32 s16, 0x178
	s_cselect_b32 s20, 0x178, 0
	s_cselect_b32 s21, 1, 0
	s_sub_i32 s16, s16, s20
	s_add_i32 s17, s17, s21
	s_cmp_ge_u32 s17, 32
	s_cselect_b32 s20, 32, 0
	s_sub_i32 s17, s17, s20
	s_waitcnt vmcnt(24)
	s_lshl_b32 s20, s18, 17
	s_lshl_b32 s21, s19, 7
	s_add_u32 s26, s14, s20
	s_addc_u32 s27, s15, 0
	s_add_u32 s26, s26, s21
	s_addc_u32 s27, s27, 0
	v_cvt_pk_bf16_f32 v20, v64, v68
	v_cvt_pk_bf16_f32 v21, v72, v76
	v_cvt_pk_bf16_f32 v22, v80, v84
	v_cvt_pk_bf16_f32 v23, v88, v92
	global_store_dwordx4 v14, v[20:23], s[26:27]
	v_cvt_pk_bf16_f32 v24, v65, v69
	v_cvt_pk_bf16_f32 v25, v73, v77
	v_cvt_pk_bf16_f32 v26, v81, v85
	v_cvt_pk_bf16_f32 v27, v89, v93
	global_store_dwordx4 v15, v[24:27], s[26:27]
	v_cvt_pk_bf16_f32 v20, v66, v70
	v_cvt_pk_bf16_f32 v21, v74, v78
	v_cvt_pk_bf16_f32 v22, v82, v86
	v_cvt_pk_bf16_f32 v23, v90, v94
	global_store_dwordx4 v16, v[20:23], s[26:27]
	v_cvt_pk_bf16_f32 v24, v67, v71
	v_cvt_pk_bf16_f32 v25, v75, v79
	v_cvt_pk_bf16_f32 v26, v83, v87
	v_cvt_pk_bf16_f32 v27, v91, v95
	global_store_dwordx4 v17, v[24:27], s[26:27]
	s_add_i32 s18, s18, 0x88
	s_add_i32 s19, s19, 1
	s_cmp_ge_u32 s18, 0x178
	s_cselect_b32 s20, 0x178, 0
	s_cselect_b32 s21, 1, 0
	s_sub_i32 s18, s18, s20
	s_add_i32 s19, s19, s21
	s_cmp_ge_u32 s19, 32
	s_cselect_b32 s20, 32, 0
	s_sub_i32 s19, s19, s20
	s_mul_i32 s20, s17, 0x2f0000
	s_lshl_b32 s21, s16, 7
	s_add_u32 s24, s12, s20
	s_addc_u32 s25, s13, 0
	s_add_u32 s24, s24, s21
	s_addc_u32 s25, s25, 0
	global_load_dwordx4 v[64:67], v6, s[24:25] nt
	global_load_dwordx4 v[68:71], v7, s[24:25] nt
	global_load_dwordx4 v[72:75], v8, s[24:25] nt
	global_load_dwordx4 v[76:79], v9, s[24:25] nt
	global_load_dwordx4 v[80:83], v10, s[24:25] nt
	global_load_dwordx4 v[84:87], v11, s[24:25] nt
	global_load_dwordx4 v[88:91], v12, s[24:25] nt
	global_load_dwordx4 v[92:95], v13, s[24:25] nt
	s_add_i32 s16, s16, 0x88
	s_add_i32 s17, s17, 1
	s_cmp_ge_u32 s16, 0x178
	s_cselect_b32 s20, 0x178, 0
	s_cselect_b32 s21, 1, 0
	s_sub_i32 s16, s16, s20
	s_add_i32 s17, s17, s21
	s_cmp_ge_u32 s17, 32
	s_cselect_b32 s20, 32, 0
	s_sub_i32 s17, s17, s20
	s_waitcnt vmcnt(24)
	s_lshl_b32 s20, s18, 17
	s_lshl_b32 s21, s19, 7
	s_add_u32 s26, s14, s20
	s_addc_u32 s27, s15, 0
	s_add_u32 s26, s26, s21
	s_addc_u32 s27, s27, 0
	v_cvt_pk_bf16_f32 v20, v96, v100
	v_cvt_pk_bf16_f32 v21, v104, v108
	v_cvt_pk_bf16_f32 v22, v112, v116
	v_cvt_pk_bf16_f32 v23, v120, v124
	global_store_dwordx4 v14, v[20:23], s[26:27]
	v_cvt_pk_bf16_f32 v24, v97, v101
	v_cvt_pk_bf16_f32 v25, v105, v109
	v_cvt_pk_bf16_f32 v26, v113, v117
	v_cvt_pk_bf16_f32 v27, v121, v125
	global_store_dwordx4 v15, v[24:27], s[26:27]
	v_cvt_pk_bf16_f32 v20, v98, v102
	v_cvt_pk_bf16_f32 v21, v106, v110
	v_cvt_pk_bf16_f32 v22, v114, v118
	v_cvt_pk_bf16_f32 v23, v122, v126
	global_store_dwordx4 v16, v[20:23], s[26:27]
	v_cvt_pk_bf16_f32 v24, v99, v103
	v_cvt_pk_bf16_f32 v25, v107, v111
	v_cvt_pk_bf16_f32 v26, v115, v119
	v_cvt_pk_bf16_f32 v27, v123, v127
	global_store_dwordx4 v17, v[24:27], s[26:27]
	s_add_i32 s18, s18, 0x88
	s_add_i32 s19, s19, 1
	s_cmp_ge_u32 s18, 0x178
	s_cselect_b32 s20, 0x178, 0
	s_cselect_b32 s21, 1, 0
	s_sub_i32 s18, s18, s20
	s_add_i32 s19, s19, s21
	s_cmp_ge_u32 s19, 32
	s_cselect_b32 s20, 32, 0
	s_sub_i32 s19, s19, s20
	s_mul_i32 s20, s17, 0x2f0000
	s_lshl_b32 s21, s16, 7
	s_add_u32 s24, s12, s20
	s_addc_u32 s25, s13, 0
	s_add_u32 s24, s24, s21
	s_addc_u32 s25, s25, 0
	global_load_dwordx4 v[96:99], v6, s[24:25] nt
	global_load_dwordx4 v[100:103], v7, s[24:25] nt
	global_load_dwordx4 v[104:107], v8, s[24:25] nt
	global_load_dwordx4 v[108:111], v9, s[24:25] nt
	global_load_dwordx4 v[112:115], v10, s[24:25] nt
	global_load_dwordx4 v[116:119], v11, s[24:25] nt
	global_load_dwordx4 v[120:123], v12, s[24:25] nt
	global_load_dwordx4 v[124:127], v13, s[24:25] nt
	s_add_i32 s16, s16, 0x88
	s_add_i32 s17, s17, 1
	s_cmp_ge_u32 s16, 0x178
	s_cselect_b32 s20, 0x178, 0
	s_cselect_b32 s21, 1, 0
	s_sub_i32 s16, s16, s20
	s_add_i32 s17, s17, s21
	s_cmp_ge_u32 s17, 32
	s_cselect_b32 s20, 32, 0
	s_sub_i32 s17, s17, s20
	s_waitcnt vmcnt(24)
	s_lshl_b32 s20, s18, 17
	s_lshl_b32 s21, s19, 7
	s_add_u32 s26, s14, s20
	s_addc_u32 s27, s15, 0
	s_add_u32 s26, s26, s21
	s_addc_u32 s27, s27, 0
	v_cvt_pk_bf16_f32 v20, v32, v36
	v_cvt_pk_bf16_f32 v21, v40, v44
	v_cvt_pk_bf16_f32 v22, v48, v52
	v_cvt_pk_bf16_f32 v23, v56, v60
	global_store_dwordx4 v14, v[20:23], s[26:27]
	v_cvt_pk_bf16_f32 v24, v33, v37
	v_cvt_pk_bf16_f32 v25, v41, v45
	v_cvt_pk_bf16_f32 v26, v49, v53
	v_cvt_pk_bf16_f32 v27, v57, v61
	global_store_dwordx4 v15, v[24:27], s[26:27]
	v_cvt_pk_bf16_f32 v20, v34, v38
	v_cvt_pk_bf16_f32 v21, v42, v46
	v_cvt_pk_bf16_f32 v22, v50, v54
	v_cvt_pk_bf16_f32 v23, v58, v62
	global_store_dwordx4 v16, v[20:23], s[26:27]
	v_cvt_pk_bf16_f32 v24, v35, v39
	v_cvt_pk_bf16_f32 v25, v43, v47
	v_cvt_pk_bf16_f32 v26, v51, v55
	v_cvt_pk_bf16_f32 v27, v59, v63
	global_store_dwordx4 v17, v[24:27], s[26:27]
	s_add_i32 s18, s18, 0x88
	s_add_i32 s19, s19, 1
	s_cmp_ge_u32 s18, 0x178
	s_cselect_b32 s20, 0x178, 0
	s_cselect_b32 s21, 1, 0
	s_sub_i32 s18, s18, s20
	s_add_i32 s19, s19, s21
	s_cmp_ge_u32 s19, 32
	s_cselect_b32 s20, 32, 0
	s_sub_i32 s19, s19, s20
	s_mul_i32 s20, s17, 0x2f0000
	s_lshl_b32 s21, s16, 7
	s_add_u32 s24, s12, s20
	s_addc_u32 s25, s13, 0
	s_add_u32 s24, s24, s21
	s_addc_u32 s25, s25, 0
	global_load_dwordx4 v[32:35], v6, s[24:25] nt
	global_load_dwordx4 v[36:39], v7, s[24:25] nt
	global_load_dwordx4 v[40:43], v8, s[24:25] nt
	global_load_dwordx4 v[44:47], v9, s[24:25] nt
	global_load_dwordx4 v[48:51], v10, s[24:25] nt
	global_load_dwordx4 v[52:55], v11, s[24:25] nt
	global_load_dwordx4 v[56:59], v12, s[24:25] nt
	global_load_dwordx4 v[60:63], v13, s[24:25] nt
	s_add_i32 s16, s16, 0x88
	s_add_i32 s17, s17, 1
	s_cmp_ge_u32 s16, 0x178
	s_cselect_b32 s20, 0x178, 0
	s_cselect_b32 s21, 1, 0
	s_sub_i32 s16, s16, s20
	s_add_i32 s17, s17, s21
	s_cmp_ge_u32 s17, 32
	s_cselect_b32 s20, 32, 0
	s_sub_i32 s17, s17, s20
	s_waitcnt vmcnt(24)
	s_lshl_b32 s20, s18, 17
	s_lshl_b32 s21, s19, 7
	s_add_u32 s26, s14, s20
	s_addc_u32 s27, s15, 0
	s_add_u32 s26, s26, s21
	s_addc_u32 s27, s27, 0
	v_cvt_pk_bf16_f32 v20, v64, v68
	v_cvt_pk_bf16_f32 v21, v72, v76
	v_cvt_pk_bf16_f32 v22, v80, v84
	v_cvt_pk_bf16_f32 v23, v88, v92
	global_store_dwordx4 v14, v[20:23], s[26:27]
	v_cvt_pk_bf16_f32 v24, v65, v69
	v_cvt_pk_bf16_f32 v25, v73, v77
	v_cvt_pk_bf16_f32 v26, v81, v85
	v_cvt_pk_bf16_f32 v27, v89, v93
	global_store_dwordx4 v15, v[24:27], s[26:27]
	v_cvt_pk_bf16_f32 v20, v66, v70
	v_cvt_pk_bf16_f32 v21, v74, v78
	v_cvt_pk_bf16_f32 v22, v82, v86
	v_cvt_pk_bf16_f32 v23, v90, v94
	global_store_dwordx4 v16, v[20:23], s[26:27]
	v_cvt_pk_bf16_f32 v24, v67, v71
	v_cvt_pk_bf16_f32 v25, v75, v79
	v_cvt_pk_bf16_f32 v26, v83, v87
	v_cvt_pk_bf16_f32 v27, v91, v95
	global_store_dwordx4 v17, v[24:27], s[26:27]
	s_add_i32 s18, s18, 0x88
	s_add_i32 s19, s19, 1
	s_cmp_ge_u32 s18, 0x178
	s_cselect_b32 s20, 0x178, 0
	s_cselect_b32 s21, 1, 0
	s_sub_i32 s18, s18, s20
	s_add_i32 s19, s19, s21
	s_cmp_ge_u32 s19, 32
	s_cselect_b32 s20, 32, 0
	s_sub_i32 s19, s19, s20
	s_mul_i32 s20, s17, 0x2f0000
	s_lshl_b32 s21, s16, 7
	s_add_u32 s24, s12, s20
	s_addc_u32 s25, s13, 0
	s_add_u32 s24, s24, s21
	s_addc_u32 s25, s25, 0
	global_load_dwordx4 v[64:67], v6, s[24:25] nt
	global_load_dwordx4 v[68:71], v7, s[24:25] nt
	global_load_dwordx4 v[72:75], v8, s[24:25] nt
	global_load_dwordx4 v[76:79], v9, s[24:25] nt
	global_load_dwordx4 v[80:83], v10, s[24:25] nt
	global_load_dwordx4 v[84:87], v11, s[24:25] nt
	global_load_dwordx4 v[88:91], v12, s[24:25] nt
	global_load_dwordx4 v[92:95], v13, s[24:25] nt
	s_add_i32 s16, s16, 0x88
	s_add_i32 s17, s17, 1
	s_cmp_ge_u32 s16, 0x178
	s_cselect_b32 s20, 0x178, 0
	s_cselect_b32 s21, 1, 0
	s_sub_i32 s16, s16, s20
	s_add_i32 s17, s17, s21
	s_cmp_ge_u32 s17, 32
	s_cselect_b32 s20, 32, 0
	s_sub_i32 s17, s17, s20
	s_waitcnt vmcnt(24)
	s_lshl_b32 s20, s18, 17
	s_lshl_b32 s21, s19, 7
	s_add_u32 s26, s14, s20
	s_addc_u32 s27, s15, 0
	s_add_u32 s26, s26, s21
	s_addc_u32 s27, s27, 0
	v_cvt_pk_bf16_f32 v20, v96, v100
	v_cvt_pk_bf16_f32 v21, v104, v108
	v_cvt_pk_bf16_f32 v22, v112, v116
	v_cvt_pk_bf16_f32 v23, v120, v124
	global_store_dwordx4 v14, v[20:23], s[26:27]
	v_cvt_pk_bf16_f32 v24, v97, v101
	v_cvt_pk_bf16_f32 v25, v105, v109
	v_cvt_pk_bf16_f32 v26, v113, v117
	v_cvt_pk_bf16_f32 v27, v121, v125
	global_store_dwordx4 v15, v[24:27], s[26:27]
	v_cvt_pk_bf16_f32 v20, v98, v102
	v_cvt_pk_bf16_f32 v21, v106, v110
	v_cvt_pk_bf16_f32 v22, v114, v118
	v_cvt_pk_bf16_f32 v23, v122, v126
	global_store_dwordx4 v16, v[20:23], s[26:27]
	v_cvt_pk_bf16_f32 v24, v99, v103
	v_cvt_pk_bf16_f32 v25, v107, v111
	v_cvt_pk_bf16_f32 v26, v115, v119
	v_cvt_pk_bf16_f32 v27, v123, v127
	global_store_dwordx4 v17, v[24:27], s[26:27]
	s_add_i32 s18, s18, 0x88
	s_add_i32 s19, s19, 1
	s_cmp_ge_u32 s18, 0x178
	s_cselect_b32 s20, 0x178, 0
	s_cselect_b32 s21, 1, 0
	s_sub_i32 s18, s18, s20
	s_add_i32 s19, s19, s21
	s_cmp_ge_u32 s19, 32
	s_cselect_b32 s20, 32, 0
	s_sub_i32 s19, s19, s20
	s_mul_i32 s20, s17, 0x2f0000
	s_lshl_b32 s21, s16, 7
	s_add_u32 s24, s12, s20
	s_addc_u32 s25, s13, 0
	s_add_u32 s24, s24, s21
	s_addc_u32 s25, s25, 0
	global_load_dwordx4 v[96:99], v6, s[24:25] nt
	global_load_dwordx4 v[100:103], v7, s[24:25] nt
	global_load_dwordx4 v[104:107], v8, s[24:25] nt
	global_load_dwordx4 v[108:111], v9, s[24:25] nt
	global_load_dwordx4 v[112:115], v10, s[24:25] nt
	global_load_dwordx4 v[116:119], v11, s[24:25] nt
	global_load_dwordx4 v[120:123], v12, s[24:25] nt
	global_load_dwordx4 v[124:127], v13, s[24:25] nt
	s_add_i32 s16, s16, 0x88
	s_add_i32 s17, s17, 1
	s_cmp_ge_u32 s16, 0x178
	s_cselect_b32 s20, 0x178, 0
	s_cselect_b32 s21, 1, 0
	s_sub_i32 s16, s16, s20
	s_add_i32 s17, s17, s21
	s_cmp_ge_u32 s17, 32
	s_cselect_b32 s20, 32, 0
	s_sub_i32 s17, s17, s20
	s_waitcnt vmcnt(24)
	s_lshl_b32 s20, s18, 17
	s_lshl_b32 s21, s19, 7
	s_add_u32 s26, s14, s20
	s_addc_u32 s27, s15, 0
	s_add_u32 s26, s26, s21
	s_addc_u32 s27, s27, 0
	v_cvt_pk_bf16_f32 v20, v32, v36
	v_cvt_pk_bf16_f32 v21, v40, v44
	v_cvt_pk_bf16_f32 v22, v48, v52
	v_cvt_pk_bf16_f32 v23, v56, v60
	global_store_dwordx4 v14, v[20:23], s[26:27]
	v_cvt_pk_bf16_f32 v24, v33, v37
	v_cvt_pk_bf16_f32 v25, v41, v45
	v_cvt_pk_bf16_f32 v26, v49, v53
	v_cvt_pk_bf16_f32 v27, v57, v61
	global_store_dwordx4 v15, v[24:27], s[26:27]
	v_cvt_pk_bf16_f32 v20, v34, v38
	v_cvt_pk_bf16_f32 v21, v42, v46
	v_cvt_pk_bf16_f32 v22, v50, v54
	v_cvt_pk_bf16_f32 v23, v58, v62
	global_store_dwordx4 v16, v[20:23], s[26:27]
	v_cvt_pk_bf16_f32 v24, v35, v39
	v_cvt_pk_bf16_f32 v25, v43, v47
	v_cvt_pk_bf16_f32 v26, v51, v55
	v_cvt_pk_bf16_f32 v27, v59, v63
	global_store_dwordx4 v17, v[24:27], s[26:27]
	s_add_i32 s18, s18, 0x88
	s_add_i32 s19, s19, 1
	s_cmp_ge_u32 s18, 0x178
	s_cselect_b32 s20, 0x178, 0
	s_cselect_b32 s21, 1, 0
	s_sub_i32 s18, s18, s20
	s_add_i32 s19, s19, s21
	s_cmp_ge_u32 s19, 32
	s_cselect_b32 s20, 32, 0
	s_sub_i32 s19, s19, s20
	s_mul_i32 s20, s17, 0x2f0000
	s_lshl_b32 s21, s16, 7
	s_add_u32 s24, s12, s20
	s_addc_u32 s25, s13, 0
	s_add_u32 s24, s24, s21
	s_addc_u32 s25, s25, 0
	global_load_dwordx4 v[32:35], v6, s[24:25] nt
	global_load_dwordx4 v[36:39], v7, s[24:25] nt
	global_load_dwordx4 v[40:43], v8, s[24:25] nt
	global_load_dwordx4 v[44:47], v9, s[24:25] nt
	global_load_dwordx4 v[48:51], v10, s[24:25] nt
	global_load_dwordx4 v[52:55], v11, s[24:25] nt
	global_load_dwordx4 v[56:59], v12, s[24:25] nt
	global_load_dwordx4 v[60:63], v13, s[24:25] nt
	s_add_i32 s16, s16, 0x88
	s_add_i32 s17, s17, 1
	s_cmp_ge_u32 s16, 0x178
	s_cselect_b32 s20, 0x178, 0
	s_cselect_b32 s21, 1, 0
	s_sub_i32 s16, s16, s20
	s_add_i32 s17, s17, s21
	s_cmp_ge_u32 s17, 32
	s_cselect_b32 s20, 32, 0
	s_sub_i32 s17, s17, s20
	s_waitcnt vmcnt(24)
	s_lshl_b32 s20, s18, 17
	s_lshl_b32 s21, s19, 7
	s_add_u32 s26, s14, s20
	s_addc_u32 s27, s15, 0
	s_add_u32 s26, s26, s21
	s_addc_u32 s27, s27, 0
	v_cvt_pk_bf16_f32 v20, v64, v68
	v_cvt_pk_bf16_f32 v21, v72, v76
	v_cvt_pk_bf16_f32 v22, v80, v84
	v_cvt_pk_bf16_f32 v23, v88, v92
	global_store_dwordx4 v14, v[20:23], s[26:27]
	v_cvt_pk_bf16_f32 v24, v65, v69
	v_cvt_pk_bf16_f32 v25, v73, v77
	v_cvt_pk_bf16_f32 v26, v81, v85
	v_cvt_pk_bf16_f32 v27, v89, v93
	global_store_dwordx4 v15, v[24:27], s[26:27]
	v_cvt_pk_bf16_f32 v20, v66, v70
	v_cvt_pk_bf16_f32 v21, v74, v78
	v_cvt_pk_bf16_f32 v22, v82, v86
	v_cvt_pk_bf16_f32 v23, v90, v94
	global_store_dwordx4 v16, v[20:23], s[26:27]
	v_cvt_pk_bf16_f32 v24, v67, v71
	v_cvt_pk_bf16_f32 v25, v75, v79
	v_cvt_pk_bf16_f32 v26, v83, v87
	v_cvt_pk_bf16_f32 v27, v91, v95
	global_store_dwordx4 v17, v[24:27], s[26:27]
	s_add_i32 s18, s18, 0x88
	s_add_i32 s19, s19, 1
	s_cmp_ge_u32 s18, 0x178
	s_cselect_b32 s20, 0x178, 0
	s_cselect_b32 s21, 1, 0
	s_sub_i32 s18, s18, s20
	s_add_i32 s19, s19, s21
	s_cmp_ge_u32 s19, 32
	s_cselect_b32 s20, 32, 0
	s_sub_i32 s19, s19, s20
	s_mul_i32 s20, s17, 0x2f0000
	s_lshl_b32 s21, s16, 7
	s_add_u32 s24, s12, s20
	s_addc_u32 s25, s13, 0
	s_add_u32 s24, s24, s21
	s_addc_u32 s25, s25, 0
	global_load_dwordx4 v[64:67], v6, s[24:25] nt
	global_load_dwordx4 v[68:71], v7, s[24:25] nt
	global_load_dwordx4 v[72:75], v8, s[24:25] nt
	global_load_dwordx4 v[76:79], v9, s[24:25] nt
	global_load_dwordx4 v[80:83], v10, s[24:25] nt
	global_load_dwordx4 v[84:87], v11, s[24:25] nt
	global_load_dwordx4 v[88:91], v12, s[24:25] nt
	global_load_dwordx4 v[92:95], v13, s[24:25] nt
	s_add_i32 s16, s16, 0x88
	s_add_i32 s17, s17, 1
	s_cmp_ge_u32 s16, 0x178
	s_cselect_b32 s20, 0x178, 0
	s_cselect_b32 s21, 1, 0
	s_sub_i32 s16, s16, s20
	s_add_i32 s17, s17, s21
	s_cmp_ge_u32 s17, 32
	s_cselect_b32 s20, 32, 0
	s_sub_i32 s17, s17, s20
	s_waitcnt vmcnt(24)
	s_lshl_b32 s20, s18, 17
	s_lshl_b32 s21, s19, 7
	s_add_u32 s26, s14, s20
	s_addc_u32 s27, s15, 0
	s_add_u32 s26, s26, s21
	s_addc_u32 s27, s27, 0
	v_cvt_pk_bf16_f32 v20, v96, v100
	v_cvt_pk_bf16_f32 v21, v104, v108
	v_cvt_pk_bf16_f32 v22, v112, v116
	v_cvt_pk_bf16_f32 v23, v120, v124
	global_store_dwordx4 v14, v[20:23], s[26:27]
	v_cvt_pk_bf16_f32 v24, v97, v101
	v_cvt_pk_bf16_f32 v25, v105, v109
	v_cvt_pk_bf16_f32 v26, v113, v117
	v_cvt_pk_bf16_f32 v27, v121, v125
	global_store_dwordx4 v15, v[24:27], s[26:27]
	v_cvt_pk_bf16_f32 v20, v98, v102
	v_cvt_pk_bf16_f32 v21, v106, v110
	v_cvt_pk_bf16_f32 v22, v114, v118
	v_cvt_pk_bf16_f32 v23, v122, v126
	global_store_dwordx4 v16, v[20:23], s[26:27]
	v_cvt_pk_bf16_f32 v24, v99, v103
	v_cvt_pk_bf16_f32 v25, v107, v111
	v_cvt_pk_bf16_f32 v26, v115, v119
	v_cvt_pk_bf16_f32 v27, v123, v127
	global_store_dwordx4 v17, v[24:27], s[26:27]
	s_add_i32 s18, s18, 0x88
	s_add_i32 s19, s19, 1
	s_cmp_ge_u32 s18, 0x178
	s_cselect_b32 s20, 0x178, 0
	s_cselect_b32 s21, 1, 0
	s_sub_i32 s18, s18, s20
	s_add_i32 s19, s19, s21
	s_cmp_ge_u32 s19, 32
	s_cselect_b32 s20, 32, 0
	s_sub_i32 s19, s19, s20
	s_mul_i32 s20, s17, 0x2f0000
	s_lshl_b32 s21, s16, 7
	s_add_u32 s24, s12, s20
	s_addc_u32 s25, s13, 0
	s_add_u32 s24, s24, s21
	s_addc_u32 s25, s25, 0
	global_load_dwordx4 v[96:99], v6, s[24:25] nt
	global_load_dwordx4 v[100:103], v7, s[24:25] nt
	global_load_dwordx4 v[104:107], v8, s[24:25] nt
	global_load_dwordx4 v[108:111], v9, s[24:25] nt
	global_load_dwordx4 v[112:115], v10, s[24:25] nt
	global_load_dwordx4 v[116:119], v11, s[24:25] nt
	global_load_dwordx4 v[120:123], v12, s[24:25] nt
	global_load_dwordx4 v[124:127], v13, s[24:25] nt
	s_add_i32 s16, s16, 0x88
	s_add_i32 s17, s17, 1
	s_cmp_ge_u32 s16, 0x178
	s_cselect_b32 s20, 0x178, 0
	s_cselect_b32 s21, 1, 0
	s_sub_i32 s16, s16, s20
	s_add_i32 s17, s17, s21
	s_cmp_ge_u32 s17, 32
	s_cselect_b32 s20, 32, 0
	s_sub_i32 s17, s17, s20
	s_waitcnt vmcnt(24)
	s_lshl_b32 s20, s18, 17
	s_lshl_b32 s21, s19, 7
	s_add_u32 s26, s14, s20
	s_addc_u32 s27, s15, 0
	s_add_u32 s26, s26, s21
	s_addc_u32 s27, s27, 0
	v_cvt_pk_bf16_f32 v20, v32, v36
	v_cvt_pk_bf16_f32 v21, v40, v44
	v_cvt_pk_bf16_f32 v22, v48, v52
	v_cvt_pk_bf16_f32 v23, v56, v60
	global_store_dwordx4 v14, v[20:23], s[26:27]
	v_cvt_pk_bf16_f32 v24, v33, v37
	v_cvt_pk_bf16_f32 v25, v41, v45
	v_cvt_pk_bf16_f32 v26, v49, v53
	v_cvt_pk_bf16_f32 v27, v57, v61
	global_store_dwordx4 v15, v[24:27], s[26:27]
	v_cvt_pk_bf16_f32 v20, v34, v38
	v_cvt_pk_bf16_f32 v21, v42, v46
	v_cvt_pk_bf16_f32 v22, v50, v54
	v_cvt_pk_bf16_f32 v23, v58, v62
	global_store_dwordx4 v16, v[20:23], s[26:27]
	v_cvt_pk_bf16_f32 v24, v35, v39
	v_cvt_pk_bf16_f32 v25, v43, v47
	v_cvt_pk_bf16_f32 v26, v51, v55
	v_cvt_pk_bf16_f32 v27, v59, v63
	global_store_dwordx4 v17, v[24:27], s[26:27]
	s_add_i32 s18, s18, 0x88
	s_add_i32 s19, s19, 1
	s_cmp_ge_u32 s18, 0x178
	s_cselect_b32 s20, 0x178, 0
	s_cselect_b32 s21, 1, 0
	s_sub_i32 s18, s18, s20
	s_add_i32 s19, s19, s21
	s_cmp_ge_u32 s19, 32
	s_cselect_b32 s20, 32, 0
	s_sub_i32 s19, s19, s20
	s_mul_i32 s20, s17, 0x2f0000
	s_lshl_b32 s21, s16, 7
	s_add_u32 s24, s12, s20
	s_addc_u32 s25, s13, 0
	s_add_u32 s24, s24, s21
	s_addc_u32 s25, s25, 0
	global_load_dwordx4 v[32:35], v6, s[24:25] nt
	global_load_dwordx4 v[36:39], v7, s[24:25] nt
	global_load_dwordx4 v[40:43], v8, s[24:25] nt
	global_load_dwordx4 v[44:47], v9, s[24:25] nt
	global_load_dwordx4 v[48:51], v10, s[24:25] nt
	global_load_dwordx4 v[52:55], v11, s[24:25] nt
	global_load_dwordx4 v[56:59], v12, s[24:25] nt
	global_load_dwordx4 v[60:63], v13, s[24:25] nt
	s_add_i32 s16, s16, 0x88
	s_add_i32 s17, s17, 1
	s_cmp_ge_u32 s16, 0x178
	s_cselect_b32 s20, 0x178, 0
	s_cselect_b32 s21, 1, 0
	s_sub_i32 s16, s16, s20
	s_add_i32 s17, s17, s21
	s_cmp_ge_u32 s17, 32
	s_cselect_b32 s20, 32, 0
	s_sub_i32 s17, s17, s20
	s_waitcnt vmcnt(24)
	s_lshl_b32 s20, s18, 17
	s_lshl_b32 s21, s19, 7
	s_add_u32 s26, s14, s20
	s_addc_u32 s27, s15, 0
	s_add_u32 s26, s26, s21
	s_addc_u32 s27, s27, 0
	v_cvt_pk_bf16_f32 v20, v64, v68
	v_cvt_pk_bf16_f32 v21, v72, v76
	v_cvt_pk_bf16_f32 v22, v80, v84
	v_cvt_pk_bf16_f32 v23, v88, v92
	global_store_dwordx4 v14, v[20:23], s[26:27]
	v_cvt_pk_bf16_f32 v24, v65, v69
	v_cvt_pk_bf16_f32 v25, v73, v77
	v_cvt_pk_bf16_f32 v26, v81, v85
	v_cvt_pk_bf16_f32 v27, v89, v93
	global_store_dwordx4 v15, v[24:27], s[26:27]
	v_cvt_pk_bf16_f32 v20, v66, v70
	v_cvt_pk_bf16_f32 v21, v74, v78
	v_cvt_pk_bf16_f32 v22, v82, v86
	v_cvt_pk_bf16_f32 v23, v90, v94
	global_store_dwordx4 v16, v[20:23], s[26:27]
	v_cvt_pk_bf16_f32 v24, v67, v71
	v_cvt_pk_bf16_f32 v25, v75, v79
	v_cvt_pk_bf16_f32 v26, v83, v87
	v_cvt_pk_bf16_f32 v27, v91, v95
	global_store_dwordx4 v17, v[24:27], s[26:27]
	s_add_i32 s18, s18, 0x88
	s_add_i32 s19, s19, 1
	s_cmp_ge_u32 s18, 0x178
	s_cselect_b32 s20, 0x178, 0
	s_cselect_b32 s21, 1, 0
	s_sub_i32 s18, s18, s20
	s_add_i32 s19, s19, s21
	s_cmp_ge_u32 s19, 32
	s_cselect_b32 s20, 32, 0
	s_sub_i32 s19, s19, s20
	s_mul_i32 s20, s17, 0x2f0000
	s_lshl_b32 s21, s16, 7
	s_add_u32 s24, s12, s20
	s_addc_u32 s25, s13, 0
	s_add_u32 s24, s24, s21
	s_addc_u32 s25, s25, 0
	global_load_dwordx4 v[64:67], v6, s[24:25] nt
	global_load_dwordx4 v[68:71], v7, s[24:25] nt
	global_load_dwordx4 v[72:75], v8, s[24:25] nt
	global_load_dwordx4 v[76:79], v9, s[24:25] nt
	global_load_dwordx4 v[80:83], v10, s[24:25] nt
	global_load_dwordx4 v[84:87], v11, s[24:25] nt
	global_load_dwordx4 v[88:91], v12, s[24:25] nt
	global_load_dwordx4 v[92:95], v13, s[24:25] nt
	s_add_i32 s16, s16, 0x88
	s_add_i32 s17, s17, 1
	s_cmp_ge_u32 s16, 0x178
	s_cselect_b32 s20, 0x178, 0
	s_cselect_b32 s21, 1, 0
	s_sub_i32 s16, s16, s20
	s_add_i32 s17, s17, s21
	s_cmp_ge_u32 s17, 32
	s_cselect_b32 s20, 32, 0
	s_sub_i32 s17, s17, s20
	s_waitcnt vmcnt(24)
	s_lshl_b32 s20, s18, 17
	s_lshl_b32 s21, s19, 7
	s_add_u32 s26, s14, s20
	s_addc_u32 s27, s15, 0
	s_add_u32 s26, s26, s21
	s_addc_u32 s27, s27, 0
	v_cvt_pk_bf16_f32 v20, v96, v100
	v_cvt_pk_bf16_f32 v21, v104, v108
	v_cvt_pk_bf16_f32 v22, v112, v116
	v_cvt_pk_bf16_f32 v23, v120, v124
	global_store_dwordx4 v14, v[20:23], s[26:27]
	v_cvt_pk_bf16_f32 v24, v97, v101
	v_cvt_pk_bf16_f32 v25, v105, v109
	v_cvt_pk_bf16_f32 v26, v113, v117
	v_cvt_pk_bf16_f32 v27, v121, v125
	global_store_dwordx4 v15, v[24:27], s[26:27]
	v_cvt_pk_bf16_f32 v20, v98, v102
	v_cvt_pk_bf16_f32 v21, v106, v110
	v_cvt_pk_bf16_f32 v22, v114, v118
	v_cvt_pk_bf16_f32 v23, v122, v126
	global_store_dwordx4 v16, v[20:23], s[26:27]
	v_cvt_pk_bf16_f32 v24, v99, v103
	v_cvt_pk_bf16_f32 v25, v107, v111
	v_cvt_pk_bf16_f32 v26, v115, v119
	v_cvt_pk_bf16_f32 v27, v123, v127
	global_store_dwordx4 v17, v[24:27], s[26:27]
	s_add_i32 s18, s18, 0x88
	s_add_i32 s19, s19, 1
	s_cmp_ge_u32 s18, 0x178
	s_cselect_b32 s20, 0x178, 0
	s_cselect_b32 s21, 1, 0
	s_sub_i32 s18, s18, s20
	s_add_i32 s19, s19, s21
	s_cmp_ge_u32 s19, 32
	s_cselect_b32 s20, 32, 0
	s_sub_i32 s19, s19, s20
	s_mul_i32 s20, s17, 0x2f0000
	s_lshl_b32 s21, s16, 7
	s_add_u32 s24, s12, s20
	s_addc_u32 s25, s13, 0
	s_add_u32 s24, s24, s21
	s_addc_u32 s25, s25, 0
	global_load_dwordx4 v[96:99], v6, s[24:25] nt
	global_load_dwordx4 v[100:103], v7, s[24:25] nt
	global_load_dwordx4 v[104:107], v8, s[24:25] nt
	global_load_dwordx4 v[108:111], v9, s[24:25] nt
	global_load_dwordx4 v[112:115], v10, s[24:25] nt
	global_load_dwordx4 v[116:119], v11, s[24:25] nt
	global_load_dwordx4 v[120:123], v12, s[24:25] nt
	global_load_dwordx4 v[124:127], v13, s[24:25] nt
	s_add_i32 s16, s16, 0x88
	s_add_i32 s17, s17, 1
	s_cmp_ge_u32 s16, 0x178
	s_cselect_b32 s20, 0x178, 0
	s_cselect_b32 s21, 1, 0
	s_sub_i32 s16, s16, s20
	s_add_i32 s17, s17, s21
	s_cmp_ge_u32 s17, 32
	s_cselect_b32 s20, 32, 0
	s_sub_i32 s17, s17, s20
	s_waitcnt vmcnt(24)
	s_lshl_b32 s20, s18, 17
	s_lshl_b32 s21, s19, 7
	s_add_u32 s26, s14, s20
	s_addc_u32 s27, s15, 0
	s_add_u32 s26, s26, s21
	s_addc_u32 s27, s27, 0
	v_cvt_pk_bf16_f32 v20, v32, v36
	v_cvt_pk_bf16_f32 v21, v40, v44
	v_cvt_pk_bf16_f32 v22, v48, v52
	v_cvt_pk_bf16_f32 v23, v56, v60
	global_store_dwordx4 v14, v[20:23], s[26:27]
	v_cvt_pk_bf16_f32 v24, v33, v37
	v_cvt_pk_bf16_f32 v25, v41, v45
	v_cvt_pk_bf16_f32 v26, v49, v53
	v_cvt_pk_bf16_f32 v27, v57, v61
	global_store_dwordx4 v15, v[24:27], s[26:27]
	v_cvt_pk_bf16_f32 v20, v34, v38
	v_cvt_pk_bf16_f32 v21, v42, v46
	v_cvt_pk_bf16_f32 v22, v50, v54
	v_cvt_pk_bf16_f32 v23, v58, v62
	global_store_dwordx4 v16, v[20:23], s[26:27]
	v_cvt_pk_bf16_f32 v24, v35, v39
	v_cvt_pk_bf16_f32 v25, v43, v47
	v_cvt_pk_bf16_f32 v26, v51, v55
	v_cvt_pk_bf16_f32 v27, v59, v63
	global_store_dwordx4 v17, v[24:27], s[26:27]
	s_add_i32 s18, s18, 0x88
	s_add_i32 s19, s19, 1
	s_cmp_ge_u32 s18, 0x178
	s_cselect_b32 s20, 0x178, 0
	s_cselect_b32 s21, 1, 0
	s_sub_i32 s18, s18, s20
	s_add_i32 s19, s19, s21
	s_cmp_ge_u32 s19, 32
	s_cselect_b32 s20, 32, 0
	s_sub_i32 s19, s19, s20
	s_mul_i32 s20, s17, 0x2f0000
	s_lshl_b32 s21, s16, 7
	s_add_u32 s24, s12, s20
	s_addc_u32 s25, s13, 0
	s_add_u32 s24, s24, s21
	s_addc_u32 s25, s25, 0
	global_load_dwordx4 v[32:35], v6, s[24:25] nt
	global_load_dwordx4 v[36:39], v7, s[24:25] nt
	global_load_dwordx4 v[40:43], v8, s[24:25] nt
	global_load_dwordx4 v[44:47], v9, s[24:25] nt
	global_load_dwordx4 v[48:51], v10, s[24:25] nt
	global_load_dwordx4 v[52:55], v11, s[24:25] nt
	global_load_dwordx4 v[56:59], v12, s[24:25] nt
	global_load_dwordx4 v[60:63], v13, s[24:25] nt
	s_add_i32 s16, s16, 0x88
	s_add_i32 s17, s17, 1
	s_cmp_ge_u32 s16, 0x178
	s_cselect_b32 s20, 0x178, 0
	s_cselect_b32 s21, 1, 0
	s_sub_i32 s16, s16, s20
	s_add_i32 s17, s17, s21
	s_cmp_ge_u32 s17, 32
	s_cselect_b32 s20, 32, 0
	s_sub_i32 s17, s17, s20
	s_waitcnt vmcnt(24)
	s_lshl_b32 s20, s18, 17
	s_lshl_b32 s21, s19, 7
	s_add_u32 s26, s14, s20
	s_addc_u32 s27, s15, 0
	s_add_u32 s26, s26, s21
	s_addc_u32 s27, s27, 0
	v_cvt_pk_bf16_f32 v20, v64, v68
	v_cvt_pk_bf16_f32 v21, v72, v76
	v_cvt_pk_bf16_f32 v22, v80, v84
	v_cvt_pk_bf16_f32 v23, v88, v92
	global_store_dwordx4 v14, v[20:23], s[26:27]
	v_cvt_pk_bf16_f32 v24, v65, v69
	v_cvt_pk_bf16_f32 v25, v73, v77
	v_cvt_pk_bf16_f32 v26, v81, v85
	v_cvt_pk_bf16_f32 v27, v89, v93
	global_store_dwordx4 v15, v[24:27], s[26:27]
	v_cvt_pk_bf16_f32 v20, v66, v70
	v_cvt_pk_bf16_f32 v21, v74, v78
	v_cvt_pk_bf16_f32 v22, v82, v86
	v_cvt_pk_bf16_f32 v23, v90, v94
	global_store_dwordx4 v16, v[20:23], s[26:27]
	v_cvt_pk_bf16_f32 v24, v67, v71
	v_cvt_pk_bf16_f32 v25, v75, v79
	v_cvt_pk_bf16_f32 v26, v83, v87
	v_cvt_pk_bf16_f32 v27, v91, v95
	global_store_dwordx4 v17, v[24:27], s[26:27]
	s_add_i32 s18, s18, 0x88
	s_add_i32 s19, s19, 1
	s_cmp_ge_u32 s18, 0x178
	s_cselect_b32 s20, 0x178, 0
	s_cselect_b32 s21, 1, 0
	s_sub_i32 s18, s18, s20
	s_add_i32 s19, s19, s21
	s_cmp_ge_u32 s19, 32
	s_cselect_b32 s20, 32, 0
	s_sub_i32 s19, s19, s20
	s_mul_i32 s20, s17, 0x2f0000
	s_lshl_b32 s21, s16, 7
	s_add_u32 s24, s12, s20
	s_addc_u32 s25, s13, 0
	s_add_u32 s24, s24, s21
	s_addc_u32 s25, s25, 0
	global_load_dwordx4 v[64:67], v6, s[24:25] nt
	global_load_dwordx4 v[68:71], v7, s[24:25] nt
	global_load_dwordx4 v[72:75], v8, s[24:25] nt
	global_load_dwordx4 v[76:79], v9, s[24:25] nt
	global_load_dwordx4 v[80:83], v10, s[24:25] nt
	global_load_dwordx4 v[84:87], v11, s[24:25] nt
	global_load_dwordx4 v[88:91], v12, s[24:25] nt
	global_load_dwordx4 v[92:95], v13, s[24:25] nt
	s_add_i32 s16, s16, 0x88
	s_add_i32 s17, s17, 1
	s_cmp_ge_u32 s16, 0x178
	s_cselect_b32 s20, 0x178, 0
	s_cselect_b32 s21, 1, 0
	s_sub_i32 s16, s16, s20
	s_add_i32 s17, s17, s21
	s_cmp_ge_u32 s17, 32
	s_cselect_b32 s20, 32, 0
	s_sub_i32 s17, s17, s20
	s_waitcnt vmcnt(24)
	s_lshl_b32 s20, s18, 17
	s_lshl_b32 s21, s19, 7
	s_add_u32 s26, s14, s20
	s_addc_u32 s27, s15, 0
	s_add_u32 s26, s26, s21
	s_addc_u32 s27, s27, 0
	v_cvt_pk_bf16_f32 v20, v96, v100
	v_cvt_pk_bf16_f32 v21, v104, v108
	v_cvt_pk_bf16_f32 v22, v112, v116
	v_cvt_pk_bf16_f32 v23, v120, v124
	global_store_dwordx4 v14, v[20:23], s[26:27]
	v_cvt_pk_bf16_f32 v24, v97, v101
	v_cvt_pk_bf16_f32 v25, v105, v109
	v_cvt_pk_bf16_f32 v26, v113, v117
	v_cvt_pk_bf16_f32 v27, v121, v125
	global_store_dwordx4 v15, v[24:27], s[26:27]
	v_cvt_pk_bf16_f32 v20, v98, v102
	v_cvt_pk_bf16_f32 v21, v106, v110
	v_cvt_pk_bf16_f32 v22, v114, v118
	v_cvt_pk_bf16_f32 v23, v122, v126
	global_store_dwordx4 v16, v[20:23], s[26:27]
	v_cvt_pk_bf16_f32 v24, v99, v103
	v_cvt_pk_bf16_f32 v25, v107, v111
	v_cvt_pk_bf16_f32 v26, v115, v119
	v_cvt_pk_bf16_f32 v27, v123, v127
	global_store_dwordx4 v17, v[24:27], s[26:27]
	s_add_i32 s18, s18, 0x88
	s_add_i32 s19, s19, 1
	s_cmp_ge_u32 s18, 0x178
	s_cselect_b32 s20, 0x178, 0
	s_cselect_b32 s21, 1, 0
	s_sub_i32 s18, s18, s20
	s_add_i32 s19, s19, s21
	s_cmp_ge_u32 s19, 32
	s_cselect_b32 s20, 32, 0
	s_sub_i32 s19, s19, s20
	s_mul_i32 s20, s17, 0x2f0000
	s_lshl_b32 s21, s16, 7
	s_add_u32 s24, s12, s20
	s_addc_u32 s25, s13, 0
	s_add_u32 s24, s24, s21
	s_addc_u32 s25, s25, 0
	global_load_dwordx4 v[96:99], v6, s[24:25] nt
	global_load_dwordx4 v[100:103], v7, s[24:25] nt
	global_load_dwordx4 v[104:107], v8, s[24:25] nt
	global_load_dwordx4 v[108:111], v9, s[24:25] nt
	global_load_dwordx4 v[112:115], v10, s[24:25] nt
	global_load_dwordx4 v[116:119], v11, s[24:25] nt
	global_load_dwordx4 v[120:123], v12, s[24:25] nt
	global_load_dwordx4 v[124:127], v13, s[24:25] nt
	s_add_i32 s16, s16, 0x88
	s_add_i32 s17, s17, 1
	s_cmp_ge_u32 s16, 0x178
	s_cselect_b32 s20, 0x178, 0
	s_cselect_b32 s21, 1, 0
	s_sub_i32 s16, s16, s20
	s_add_i32 s17, s17, s21
	s_cmp_ge_u32 s17, 32
	s_cselect_b32 s20, 32, 0
	s_sub_i32 s17, s17, s20
	s_waitcnt vmcnt(24)
	s_lshl_b32 s20, s18, 17
	s_lshl_b32 s21, s19, 7
	s_add_u32 s26, s14, s20
	s_addc_u32 s27, s15, 0
	s_add_u32 s26, s26, s21
	s_addc_u32 s27, s27, 0
	v_cvt_pk_bf16_f32 v20, v32, v36
	v_cvt_pk_bf16_f32 v21, v40, v44
	v_cvt_pk_bf16_f32 v22, v48, v52
	v_cvt_pk_bf16_f32 v23, v56, v60
	global_store_dwordx4 v14, v[20:23], s[26:27]
	v_cvt_pk_bf16_f32 v24, v33, v37
	v_cvt_pk_bf16_f32 v25, v41, v45
	v_cvt_pk_bf16_f32 v26, v49, v53
	v_cvt_pk_bf16_f32 v27, v57, v61
	global_store_dwordx4 v15, v[24:27], s[26:27]
	v_cvt_pk_bf16_f32 v20, v34, v38
	v_cvt_pk_bf16_f32 v21, v42, v46
	v_cvt_pk_bf16_f32 v22, v50, v54
	v_cvt_pk_bf16_f32 v23, v58, v62
	global_store_dwordx4 v16, v[20:23], s[26:27]
	v_cvt_pk_bf16_f32 v24, v35, v39
	v_cvt_pk_bf16_f32 v25, v43, v47
	v_cvt_pk_bf16_f32 v26, v51, v55
	v_cvt_pk_bf16_f32 v27, v59, v63
	global_store_dwordx4 v17, v[24:27], s[26:27]
	s_add_i32 s18, s18, 0x88
	s_add_i32 s19, s19, 1
	s_cmp_ge_u32 s18, 0x178
	s_cselect_b32 s20, 0x178, 0
	s_cselect_b32 s21, 1, 0
	s_sub_i32 s18, s18, s20
	s_add_i32 s19, s19, s21
	s_cmp_ge_u32 s19, 32
	s_cselect_b32 s20, 32, 0
	s_sub_i32 s19, s19, s20
	s_mul_i32 s20, s17, 0x2f0000
	s_lshl_b32 s21, s16, 7
	s_add_u32 s24, s12, s20
	s_addc_u32 s25, s13, 0
	s_add_u32 s24, s24, s21
	s_addc_u32 s25, s25, 0
	global_load_dwordx4 v[32:35], v6, s[24:25] nt
	global_load_dwordx4 v[36:39], v7, s[24:25] nt
	global_load_dwordx4 v[40:43], v8, s[24:25] nt
	global_load_dwordx4 v[44:47], v9, s[24:25] nt
	global_load_dwordx4 v[48:51], v10, s[24:25] nt
	global_load_dwordx4 v[52:55], v11, s[24:25] nt
	global_load_dwordx4 v[56:59], v12, s[24:25] nt
	global_load_dwordx4 v[60:63], v13, s[24:25] nt
	s_add_i32 s16, s16, 0x88
	s_add_i32 s17, s17, 1
	s_cmp_ge_u32 s16, 0x178
	s_cselect_b32 s20, 0x178, 0
	s_cselect_b32 s21, 1, 0
	s_sub_i32 s16, s16, s20
	s_add_i32 s17, s17, s21
	s_cmp_ge_u32 s17, 32
	s_cselect_b32 s20, 32, 0
	s_sub_i32 s17, s17, s20
	s_waitcnt vmcnt(24)
	s_lshl_b32 s20, s18, 17
	s_lshl_b32 s21, s19, 7
	s_add_u32 s26, s14, s20
	s_addc_u32 s27, s15, 0
	s_add_u32 s26, s26, s21
	s_addc_u32 s27, s27, 0
	v_cvt_pk_bf16_f32 v20, v64, v68
	v_cvt_pk_bf16_f32 v21, v72, v76
	v_cvt_pk_bf16_f32 v22, v80, v84
	v_cvt_pk_bf16_f32 v23, v88, v92
	global_store_dwordx4 v14, v[20:23], s[26:27]
	v_cvt_pk_bf16_f32 v24, v65, v69
	v_cvt_pk_bf16_f32 v25, v73, v77
	v_cvt_pk_bf16_f32 v26, v81, v85
	v_cvt_pk_bf16_f32 v27, v89, v93
	global_store_dwordx4 v15, v[24:27], s[26:27]
	v_cvt_pk_bf16_f32 v20, v66, v70
	v_cvt_pk_bf16_f32 v21, v74, v78
	v_cvt_pk_bf16_f32 v22, v82, v86
	v_cvt_pk_bf16_f32 v23, v90, v94
	global_store_dwordx4 v16, v[20:23], s[26:27]
	v_cvt_pk_bf16_f32 v24, v67, v71
	v_cvt_pk_bf16_f32 v25, v75, v79
	v_cvt_pk_bf16_f32 v26, v83, v87
	v_cvt_pk_bf16_f32 v27, v91, v95
	global_store_dwordx4 v17, v[24:27], s[26:27]
	s_add_i32 s18, s18, 0x88
	s_add_i32 s19, s19, 1
	s_cmp_ge_u32 s18, 0x178
	s_cselect_b32 s20, 0x178, 0
	s_cselect_b32 s21, 1, 0
	s_sub_i32 s18, s18, s20
	s_add_i32 s19, s19, s21
	s_cmp_ge_u32 s19, 32
	s_cselect_b32 s20, 32, 0
	s_sub_i32 s19, s19, s20
	s_mul_i32 s20, s17, 0x2f0000
	s_lshl_b32 s21, s16, 7
	s_add_u32 s24, s12, s20
	s_addc_u32 s25, s13, 0
	s_add_u32 s24, s24, s21
	s_addc_u32 s25, s25, 0
	global_load_dwordx4 v[64:67], v6, s[24:25] nt
	global_load_dwordx4 v[68:71], v7, s[24:25] nt
	global_load_dwordx4 v[72:75], v8, s[24:25] nt
	global_load_dwordx4 v[76:79], v9, s[24:25] nt
	global_load_dwordx4 v[80:83], v10, s[24:25] nt
	global_load_dwordx4 v[84:87], v11, s[24:25] nt
	global_load_dwordx4 v[88:91], v12, s[24:25] nt
	global_load_dwordx4 v[92:95], v13, s[24:25] nt
	s_add_i32 s16, s16, 0x88
	s_add_i32 s17, s17, 1
	s_cmp_ge_u32 s16, 0x178
	s_cselect_b32 s20, 0x178, 0
	s_cselect_b32 s21, 1, 0
	s_sub_i32 s16, s16, s20
	s_add_i32 s17, s17, s21
	s_cmp_ge_u32 s17, 32
	s_cselect_b32 s20, 32, 0
	s_sub_i32 s17, s17, s20
	s_waitcnt vmcnt(24)
	s_lshl_b32 s20, s18, 17
	s_lshl_b32 s21, s19, 7
	s_add_u32 s26, s14, s20
	s_addc_u32 s27, s15, 0
	s_add_u32 s26, s26, s21
	s_addc_u32 s27, s27, 0
	v_cvt_pk_bf16_f32 v20, v96, v100
	v_cvt_pk_bf16_f32 v21, v104, v108
	v_cvt_pk_bf16_f32 v22, v112, v116
	v_cvt_pk_bf16_f32 v23, v120, v124
	global_store_dwordx4 v14, v[20:23], s[26:27]
	v_cvt_pk_bf16_f32 v24, v97, v101
	v_cvt_pk_bf16_f32 v25, v105, v109
	v_cvt_pk_bf16_f32 v26, v113, v117
	v_cvt_pk_bf16_f32 v27, v121, v125
	global_store_dwordx4 v15, v[24:27], s[26:27]
	v_cvt_pk_bf16_f32 v20, v98, v102
	v_cvt_pk_bf16_f32 v21, v106, v110
	v_cvt_pk_bf16_f32 v22, v114, v118
	v_cvt_pk_bf16_f32 v23, v122, v126
	global_store_dwordx4 v16, v[20:23], s[26:27]
	v_cvt_pk_bf16_f32 v24, v99, v103
	v_cvt_pk_bf16_f32 v25, v107, v111
	v_cvt_pk_bf16_f32 v26, v115, v119
	v_cvt_pk_bf16_f32 v27, v123, v127
	global_store_dwordx4 v17, v[24:27], s[26:27]
	s_add_i32 s18, s18, 0x88
	s_add_i32 s19, s19, 1
	s_cmp_ge_u32 s18, 0x178
	s_cselect_b32 s20, 0x178, 0
	s_cselect_b32 s21, 1, 0
	s_sub_i32 s18, s18, s20
	s_add_i32 s19, s19, s21
	s_cmp_ge_u32 s19, 32
	s_cselect_b32 s20, 32, 0
	s_sub_i32 s19, s19, s20
.Lwin1_done:
.LBB0_46:
	v_readlane_b32 s4, v254, 10
	v_readlane_b32 s5, v254, 11
	s_andn2_b64 vcc, exec, s[4:5]
	s_nop 0
	v_cndmask_b32_e64 v0, 0, 1, s[4:5]
	v_cmp_ne_u32_e64 s[6:7], 1, v0
	s_cbranch_vccnz .LBB0_72
	s_add_i32 s41, s50, s84
	s_cmp_gt_i32 s41, 0x185ff
	s_cbranch_scc1 .LBB0_71
	s_load_dwordx8 s[12:19], s[8:9], 0x80
	s_load_dwordx4 s[28:31], s[8:9], 0xa0
	v_readlane_b32 s8, v255, 60
	v_readlane_b32 s9, v255, 61
	s_mov_b32 s9, s87
	s_lshl_b64 s[4:5], s[8:9], 28
	s_waitcnt lgkmcnt(0)
	s_add_u32 s3, s12, s4
	s_addc_u32 s20, s13, s5
	s_add_u32 s21, s14, s4
	s_addc_u32 s22, s15, s5
	s_add_u32 s23, s16, s4
	s_mov_b32 s4, s8
	s_addc_u32 s24, s17, s5
	v_writelane_b32 v255, s4, 60
	s_mov_b64 s[14:15], -1
	s_nop 0
	v_writelane_b32 v255, s5, 61
	s_lshl_b64 s[4:5], s[8:9], 22
	s_add_u32 s25, s18, s4
	s_addc_u32 s26, s19, s5
	s_add_u32 s27, s28, s4
	s_addc_u32 s28, s29, s5
	s_add_u32 s29, s30, s4
	s_mul_hi_i32 s4, s41, 0x2aaaaaab
	s_addc_u32 s30, s31, s5
	s_lshr_b32 s5, s4, 31
	s_ashr_i32 s4, s4, 8
	s_add_i32 s12, s4, s5
	s_mul_i32 s4, s12, 0x600
	s_sub_i32 s16, s41, s4
	s_ashr_i32 s17, s16, 9
	s_cmp_gt_i32 s17, 1
	s_cbranch_scc0 .LBB0_50
	s_ashr_i32 s13, s12, 31
	s_lshl_b64 s[4:5], s[12:13], 22
	s_add_u32 s4, s23, s4
	s_addc_u32 s5, s24, s5
	s_cmp_lt_i32 s41, 0x18000
	s_cselect_b32 s5, s5, s30
	s_cselect_b32 s4, s4, s29
	s_and_b32 s14, s16, 0x1c0
	s_lshl_b32 s8, s16, 5
	s_and_b32 s15, s8, 0x7e0
	s_lshl_b32 s8, s14, 13
	s_add_u32 s4, s4, s8
	s_addc_u32 s5, s5, 0
	s_lshl_b32 s8, s15, 2
	s_add_u32 s4, s4, s8
	s_addc_u32 s5, s5, 0
	s_lshl_b64 s[8:9], s[12:13], 21
	s_add_u32 s8, s10, s8
	s_addc_u32 s9, s11, s9
	s_lshl_b32 s13, s15, 10
	s_add_u32 s8, s8, s13
	s_addc_u32 s9, s9, 0
	s_lshl_b32 s13, s14, 1
	s_add_u32 s8, s8, s13
	s_addc_u32 s9, s9, 0
	s_add_u32 s8, s8, 0x19400000
	s_addc_u32 s9, s9, 0
	s_mov_b64 s[14:15], 0

.LBB0_87:
	s_andn2_b64 vcc, exec, s[22:23]
	s_cbranch_vccnz .LBB0_90
	s_add_u32 s46, s46, 0x80
	s_addc_u32 s47, s47, 0
	s_add_u32 s27, s48, 0x100
	s_addc_u32 s29, s49, 0
	s_mov_b32 s4, 0
	s_add_i32 s48, s4, 2
	s_add_u32 s49, s46, 0x80
	s_addc_u32 s5, s47, 0
	s_add_i32 s77, 0, 0x10000
	s_cmp_eq_u32 s72, s4
	s_cselect_b32 s5, s43, s5
	s_cselect_b32 s4, s42, s49
	v_add_u32_e32 v149, s77, v145
	s_cselect_b32 s83, s45, s29
	s_cselect_b32 s82, s44, s27
	s_add_i32 s49, 0, 0x14000
	ds_read_b128 v[140:143], v149
	ds_read_b128 v[150:153], v149 offset:1024
	ds_read_b128 v[154:157], v149 offset:2048
	ds_read_b128 v[158:161], v149 offset:3072
	v_add_u32_e32 v149, s49, v145
	ds_read_b128 v[162:165], v149
	ds_read_b128 v[166:169], v149 offset:1024
	ds_read_b128 v[170:173], v149 offset:2048
	ds_read_b128 v[174:177], v149 offset:3072
	v_lshl_add_u64 v[214:215], s[46:47], 0, v[136:137]
	s_add_i32 m0, s37, 0xc000
	ds_read_b128 v[178:181], v148
	ds_read_b128 v[182:185], v148 offset:1024
	ds_read_b128 v[186:189], v148 offset:2048
	ds_read_b128 v[190:193], v148 offset:3072
	ds_read_b128 v[194:197], v148 offset:4096
	ds_read_b128 v[202:205], v148 offset:5120
	ds_read_b128 v[206:209], v148 offset:6144
	ds_read_b128 v[210:213], v148 offset:7168
	global_load_lds_dwordx4 v[214:215], off
	v_lshl_add_u64 v[214:215], s[46:47], 0, v[138:139]
	s_add_i32 m0, s37, 0xe000
	s_nop 0
	global_load_lds_dwordx4 v[214:215], off
	s_waitcnt vmcnt(8)
	s_waitcnt lgkmcnt(0)
	s_barrier
	s_setprio 1
	s_waitcnt lgkmcnt(0)
	v_mfma_f32_16x16x32_bf16 v[122:125], v[140:143], v[178:181], 0
	v_mfma_f32_16x16x32_bf16 v[126:129], v[154:157], v[178:181], 0
	v_mfma_f32_16x16x32_bf16 v[110:113], v[140:143], v[186:189], 0
	v_mfma_f32_16x16x32_bf16 v[106:109], v[154:157], v[186:189], 0
	v_mfma_f32_16x16x32_bf16 v[94:97], v[140:143], v[194:197], 0
	v_mfma_f32_16x16x32_bf16 v[90:93], v[154:157], v[194:197], 0
	v_mfma_f32_16x16x32_bf16 v[78:81], v[140:143], v[206:209], 0
	v_mfma_f32_16x16x32_bf16 v[74:77], v[154:157], v[206:209], 0
	v_mfma_f32_16x16x32_bf16 v[122:125], v[150:153], v[182:185], v[122:125]
	v_mfma_f32_16x16x32_bf16 v[126:129], v[158:161], v[182:185], v[126:129]
	v_mfma_f32_16x16x32_bf16 v[110:113], v[150:153], v[190:193], v[110:113]
	v_mfma_f32_16x16x32_bf16 v[106:109], v[158:161], v[190:193], v[106:109]
	v_mfma_f32_16x16x32_bf16 v[94:97], v[150:153], v[202:205], v[94:97]
	v_mfma_f32_16x16x32_bf16 v[90:93], v[158:161], v[202:205], v[90:93]
	v_mfma_f32_16x16x32_bf16 v[78:81], v[150:153], v[210:213], v[78:81]
	v_mfma_f32_16x16x32_bf16 v[74:77], v[158:161], v[210:213], v[74:77]
	s_setprio 0
	s_setprio 1
	v_mfma_f32_16x16x32_bf16 v[118:121], v[162:165], v[178:181], 0
	v_mfma_f32_16x16x32_bf16 v[114:117], v[170:173], v[178:181], 0
	v_mfma_f32_16x16x32_bf16 v[102:105], v[162:165], v[186:189], 0
	v_mfma_f32_16x16x32_bf16 v[98:101], v[170:173], v[186:189], 0
	v_mfma_f32_16x16x32_bf16 v[86:89], v[162:165], v[194:197], 0
	v_mfma_f32_16x16x32_bf16 v[82:85], v[170:173], v[194:197], 0
	v_mfma_f32_16x16x32_bf16 v[70:73], v[162:165], v[206:209], 0
	v_mfma_f32_16x16x32_bf16 v[66:69], v[170:173], v[206:209], 0
	v_mfma_f32_16x16x32_bf16 v[118:121], v[166:169], v[182:185], v[118:121]
	v_mfma_f32_16x16x32_bf16 v[114:117], v[174:177], v[182:185], v[114:117]
	v_mfma_f32_16x16x32_bf16 v[102:105], v[166:169], v[190:193], v[102:105]
	v_mfma_f32_16x16x32_bf16 v[98:101], v[174:177], v[190:193], v[98:101]
	v_mfma_f32_16x16x32_bf16 v[86:89], v[166:169], v[202:205], v[86:89]
	v_mfma_f32_16x16x32_bf16 v[82:85], v[174:177], v[202:205], v[82:85]
	v_mfma_f32_16x16x32_bf16 v[70:73], v[166:169], v[210:213], v[70:73]
	v_mfma_f32_16x16x32_bf16 v[66:69], v[174:177], v[210:213], v[66:69]
	s_setprio 0
	s_barrier
	s_add_i32 s77, s77, s51
	v_lshl_add_u64 v[214:215], s[82:83], 0, v[0:1]
	s_mov_b32 m0, s77
	ds_read_b128 v[178:181], v148 offset:16384
	ds_read_b128 v[182:185], v148 offset:17408
	ds_read_b128 v[186:189], v148 offset:18432
	ds_read_b128 v[190:193], v148 offset:19456
	ds_read_b128 v[194:197], v148 offset:20480
	ds_read_b128 v[202:205], v148 offset:21504
	ds_read_b128 v[206:209], v148 offset:22528
	ds_read_b128 v[210:213], v148 offset:23552
	global_load_lds_dwordx4 v[214:215], off
	s_add_i32 m0, s77, 0x2000
	v_lshl_add_u64 v[216:217], s[82:83], 0, v[130:131]
	s_add_u32 s82, s82, s14
	s_addc_u32 s83, s83, s15
	s_add_i32 s49, s49, s51
	global_load_lds_dwordx4 v[216:217], off
	v_lshl_add_u64 v[218:219], s[82:83], 0, v[0:1]
	s_mov_b32 m0, s49
	v_lshl_add_u64 v[220:221], s[82:83], 0, v[130:131]
	global_load_lds_dwordx4 v[218:219], off
	s_add_i32 m0, s49, 0x2000
	v_lshl_add_u64 v[234:235], s[4:5], 0, v[132:133]
	global_load_lds_dwordx4 v[220:221], off
	s_mov_b32 m0, s37
	v_lshl_add_u64 v[236:237], s[4:5], 0, v[134:135]
	global_load_lds_dwordx4 v[234:235], off
	s_mov_b32 m0, s41
	s_nop 0
	global_load_lds_dwordx4 v[236:237], off
	s_waitcnt vmcnt(8)
	s_waitcnt lgkmcnt(0)
	s_barrier
	s_setprio 1
	s_waitcnt lgkmcnt(0)
	v_mfma_f32_16x16x32_bf16 v[62:65], v[140:143], v[178:181], 0
	v_mfma_f32_16x16x32_bf16 v[58:61], v[154:157], v[178:181], 0
	v_mfma_f32_16x16x32_bf16 v[46:49], v[140:143], v[186:189], 0
	v_mfma_f32_16x16x32_bf16 v[42:45], v[154:157], v[186:189], 0
	v_mfma_f32_16x16x32_bf16 v[30:33], v[140:143], v[194:197], 0
	v_mfma_f32_16x16x32_bf16 v[26:29], v[154:157], v[194:197], 0
	v_mfma_f32_16x16x32_bf16 v[14:17], v[140:143], v[206:209], 0
	v_mfma_f32_16x16x32_bf16 v[10:13], v[154:157], v[206:209], 0
	v_mfma_f32_16x16x32_bf16 v[62:65], v[150:153], v[182:185], v[62:65]
	v_mfma_f32_16x16x32_bf16 v[58:61], v[158:161], v[182:185], v[58:61]
	v_mfma_f32_16x16x32_bf16 v[46:49], v[150:153], v[190:193], v[46:49]
	v_mfma_f32_16x16x32_bf16 v[42:45], v[158:161], v[190:193], v[42:45]
	v_mfma_f32_16x16x32_bf16 v[30:33], v[150:153], v[202:205], v[30:33]
	v_mfma_f32_16x16x32_bf16 v[26:29], v[158:161], v[202:205], v[26:29]
	v_mfma_f32_16x16x32_bf16 v[14:17], v[150:153], v[210:213], v[14:17]
	v_mfma_f32_16x16x32_bf16 v[10:13], v[158:161], v[210:213], v[10:13]
	s_setprio 0
	s_setprio 1
	v_mfma_f32_16x16x32_bf16 v[54:57], v[162:165], v[178:181], 0
	v_mfma_f32_16x16x32_bf16 v[50:53], v[170:173], v[178:181], 0
	v_mfma_f32_16x16x32_bf16 v[38:41], v[162:165], v[186:189], 0
	v_mfma_f32_16x16x32_bf16 v[34:37], v[170:173], v[186:189], 0
	v_mfma_f32_16x16x32_bf16 v[22:25], v[162:165], v[194:197], 0
	v_mfma_f32_16x16x32_bf16 v[18:21], v[170:173], v[194:197], 0
	v_mfma_f32_16x16x32_bf16 v[6:9], v[162:165], v[206:209], 0
	v_mfma_f32_16x16x32_bf16 v[2:5], v[170:173], v[206:209], 0
	v_mfma_f32_16x16x32_bf16 v[54:57], v[166:169], v[182:185], v[54:57]
	v_mfma_f32_16x16x32_bf16 v[50:53], v[174:177], v[182:185], v[50:53]
	v_mfma_f32_16x16x32_bf16 v[38:41], v[166:169], v[190:193], v[38:41]
	v_mfma_f32_16x16x32_bf16 v[34:37], v[174:177], v[190:193], v[34:37]
	v_mfma_f32_16x16x32_bf16 v[22:25], v[166:169], v[202:205], v[22:25]
	v_mfma_f32_16x16x32_bf16 v[18:21], v[174:177], v[202:205], v[18:21]
	v_mfma_f32_16x16x32_bf16 v[6:9], v[166:169], v[210:213], v[6:9]
	v_mfma_f32_16x16x32_bf16 v[2:5], v[174:177], v[210:213], v[2:5]
	s_setprio 0
	s_barrier
	s_add_i32 s49, 0, 0x18000
	v_add_u32_e32 v149, s49, v145
	s_add_i32 s77, 0, 0x1c000
	ds_read_b128 v[140:143], v149
	ds_read_b128 v[150:153], v149 offset:1024
	ds_read_b128 v[154:157], v149 offset:2048
	ds_read_b128 v[158:161], v149 offset:3072
	v_add_u32_e32 v149, s77, v145
	ds_read_b128 v[162:165], v149
	ds_read_b128 v[166:169], v149 offset:1024
	ds_read_b128 v[170:173], v149 offset:2048
	ds_read_b128 v[174:177], v149 offset:3072
	s_add_u32 s4, s4, s14
	s_addc_u32 s5, s5, s15
	s_mov_b32 m0, s67
	v_lshl_add_u64 v[238:239], s[4:5], 0, v[132:133]
	ds_read_b128 v[178:181], v148 offset:32768
	ds_read_b128 v[182:185], v148 offset:33792
	ds_read_b128 v[186:189], v148 offset:34816
	ds_read_b128 v[190:193], v148 offset:35840
	ds_read_b128 v[194:197], v148 offset:36864
	ds_read_b128 v[202:205], v148 offset:37888
	ds_read_b128 v[206:209], v148 offset:38912
	ds_read_b128 v[210:213], v148 offset:39936
	global_load_lds_dwordx4 v[238:239], off
	v_lshl_add_u64 v[238:239], s[4:5], 0, v[134:135]
	s_mov_b32 m0, s68
	s_nop 0
	global_load_lds_dwordx4 v[238:239], off
	s_waitcnt vmcnt(8)
	s_waitcnt lgkmcnt(0)
	s_barrier
	s_setprio 1
	s_waitcnt lgkmcnt(0)
	v_mfma_f32_16x16x32_bf16 v[122:125], v[140:143], v[178:181], v[122:125]
	v_mfma_f32_16x16x32_bf16 v[126:129], v[154:157], v[178:181], v[126:129]
	v_mfma_f32_16x16x32_bf16 v[110:113], v[140:143], v[186:189], v[110:113]
	v_mfma_f32_16x16x32_bf16 v[106:109], v[154:157], v[186:189], v[106:109]
	v_mfma_f32_16x16x32_bf16 v[94:97], v[140:143], v[194:197], v[94:97]
	v_mfma_f32_16x16x32_bf16 v[90:93], v[154:157], v[194:197], v[90:93]
	v_mfma_f32_16x16x32_bf16 v[78:81], v[140:143], v[206:209], v[78:81]
	v_mfma_f32_16x16x32_bf16 v[74:77], v[154:157], v[206:209], v[74:77]
	v_mfma_f32_16x16x32_bf16 v[122:125], v[150:153], v[182:185], v[122:125]
	v_mfma_f32_16x16x32_bf16 v[126:129], v[158:161], v[182:185], v[126:129]
	v_mfma_f32_16x16x32_bf16 v[110:113], v[150:153], v[190:193], v[110:113]
	v_mfma_f32_16x16x32_bf16 v[106:109], v[158:161], v[190:193], v[106:109]
	v_mfma_f32_16x16x32_bf16 v[94:97], v[150:153], v[202:205], v[94:97]
	v_mfma_f32_16x16x32_bf16 v[90:93], v[158:161], v[202:205], v[90:93]
	v_mfma_f32_16x16x32_bf16 v[78:81], v[150:153], v[210:213], v[78:81]
	v_mfma_f32_16x16x32_bf16 v[74:77], v[158:161], v[210:213], v[74:77]
	s_setprio 0
	s_setprio 1
	v_mfma_f32_16x16x32_bf16 v[118:121], v[162:165], v[178:181], v[118:121]
	v_mfma_f32_16x16x32_bf16 v[114:117], v[170:173], v[178:181], v[114:117]
	v_mfma_f32_16x16x32_bf16 v[102:105], v[162:165], v[186:189], v[102:105]
	v_mfma_f32_16x16x32_bf16 v[98:101], v[170:173], v[186:189], v[98:101]
	v_mfma_f32_16x16x32_bf16 v[86:89], v[162:165], v[194:197], v[86:89]
	v_mfma_f32_16x16x32_bf16 v[82:85], v[170:173], v[194:197], v[82:85]
	v_mfma_f32_16x16x32_bf16 v[70:73], v[162:165], v[206:209], v[70:73]
	v_mfma_f32_16x16x32_bf16 v[66:69], v[170:173], v[206:209], v[66:69]
	v_mfma_f32_16x16x32_bf16 v[118:121], v[166:169], v[182:185], v[118:121]
	v_mfma_f32_16x16x32_bf16 v[114:117], v[174:177], v[182:185], v[114:117]
	v_mfma_f32_16x16x32_bf16 v[102:105], v[166:169], v[190:193], v[102:105]
	v_mfma_f32_16x16x32_bf16 v[98:101], v[174:177], v[190:193], v[98:101]
	v_mfma_f32_16x16x32_bf16 v[86:89], v[166:169], v[202:205], v[86:89]
	v_mfma_f32_16x16x32_bf16 v[82:85], v[174:177], v[202:205], v[82:85]
	v_mfma_f32_16x16x32_bf16 v[70:73], v[166:169], v[210:213], v[70:73]
	v_mfma_f32_16x16x32_bf16 v[66:69], v[174:177], v[210:213], v[66:69]
	s_setprio 0
	s_barrier
	s_add_i32 s4, s49, s51
	v_lshl_add_u64 v[214:215], v[214:215], 0, s[94:95]
	s_mov_b32 m0, s4
	ds_read_b128 v[178:181], v148 offset:49152
	ds_read_b128 v[182:185], v148 offset:50176
	ds_read_b128 v[186:189], v148 offset:51200
	ds_read_b128 v[190:193], v148 offset:52224
	ds_read_b128 v[194:197], v148 offset:53248
	ds_read_b128 v[202:205], v148 offset:54272
	ds_read_b128 v[206:209], v148 offset:55296
	ds_read_b128 v[210:213], v148 offset:56320
	global_load_lds_dwordx4 v[214:215], off
	v_lshl_add_u64 v[214:215], v[216:217], 0, s[94:95]
	s_add_i32 m0, s4, 0x2000
	s_add_i32 s4, s77, s51
	global_load_lds_dwordx4 v[214:215], off
	v_lshl_add_u64 v[214:215], v[218:219], 0, s[94:95]
	s_mov_b32 m0, s4
	s_nop 0
	global_load_lds_dwordx4 v[214:215], off
	v_lshl_add_u64 v[214:215], v[220:221], 0, s[94:95]
	s_add_i32 m0, s4, 0x2000
	s_nop 0
	global_load_lds_dwordx4 v[214:215], off
	v_lshl_add_u64 v[214:215], v[234:235], 0, s[94:95]
	s_mov_b32 m0, s69
	s_nop 0
	global_load_lds_dwordx4 v[214:215], off
	v_lshl_add_u64 v[214:215], v[236:237], 0, s[94:95]
	s_mov_b32 m0, s70
	s_nop 0
	global_load_lds_dwordx4 v[214:215], off
	s_waitcnt vmcnt(8)
	s_waitcnt lgkmcnt(0)
	s_barrier
	s_setprio 1
	s_waitcnt lgkmcnt(0)
	v_mfma_f32_16x16x32_bf16 v[62:65], v[140:143], v[178:181], v[62:65]
	v_mfma_f32_16x16x32_bf16 v[58:61], v[154:157], v[178:181], v[58:61]
	v_mfma_f32_16x16x32_bf16 v[46:49], v[140:143], v[186:189], v[46:49]
	v_mfma_f32_16x16x32_bf16 v[42:45], v[154:157], v[186:189], v[42:45]
	v_mfma_f32_16x16x32_bf16 v[30:33], v[140:143], v[194:197], v[30:33]
	v_mfma_f32_16x16x32_bf16 v[26:29], v[154:157], v[194:197], v[26:29]
	v_mfma_f32_16x16x32_bf16 v[14:17], v[140:143], v[206:209], v[14:17]
	v_mfma_f32_16x16x32_bf16 v[10:13], v[154:157], v[206:209], v[10:13]
	v_mfma_f32_16x16x32_bf16 v[62:65], v[150:153], v[182:185], v[62:65]
	v_mfma_f32_16x16x32_bf16 v[58:61], v[158:161], v[182:185], v[58:61]
	v_mfma_f32_16x16x32_bf16 v[46:49], v[150:153], v[190:193], v[46:49]
	v_mfma_f32_16x16x32_bf16 v[42:45], v[158:161], v[190:193], v[42:45]
	v_mfma_f32_16x16x32_bf16 v[30:33], v[150:153], v[202:205], v[30:33]
	v_mfma_f32_16x16x32_bf16 v[26:29], v[158:161], v[202:205], v[26:29]
	v_mfma_f32_16x16x32_bf16 v[14:17], v[150:153], v[210:213], v[14:17]
	v_mfma_f32_16x16x32_bf16 v[10:13], v[158:161], v[210:213], v[10:13]
	s_setprio 0
	s_setprio 1
	v_mfma_f32_16x16x32_bf16 v[54:57], v[162:165], v[178:181], v[54:57]
	v_mfma_f32_16x16x32_bf16 v[50:53], v[170:173], v[178:181], v[50:53]
	v_mfma_f32_16x16x32_bf16 v[38:41], v[162:165], v[186:189], v[38:41]
	v_mfma_f32_16x16x32_bf16 v[34:37], v[170:173], v[186:189], v[34:37]
	v_mfma_f32_16x16x32_bf16 v[22:25], v[162:165], v[194:197], v[22:25]
	v_mfma_f32_16x16x32_bf16 v[18:21], v[170:173], v[194:197], v[18:21]
	v_mfma_f32_16x16x32_bf16 v[6:9], v[162:165], v[206:209], v[6:9]
	v_mfma_f32_16x16x32_bf16 v[2:5], v[170:173], v[206:209], v[2:5]
	v_mfma_f32_16x16x32_bf16 v[54:57], v[166:169], v[182:185], v[54:57]
	v_mfma_f32_16x16x32_bf16 v[50:53], v[174:177], v[182:185], v[50:53]
	v_mfma_f32_16x16x32_bf16 v[38:41], v[166:169], v[190:193], v[38:41]
	v_mfma_f32_16x16x32_bf16 v[34:37], v[174:177], v[190:193], v[34:37]
	v_mfma_f32_16x16x32_bf16 v[22:25], v[166:169], v[202:205], v[22:25]
	v_mfma_f32_16x16x32_bf16 v[18:21], v[174:177], v[202:205], v[18:21]
	v_mfma_f32_16x16x32_bf16 v[6:9], v[166:169], v[210:213], v[6:9]
	v_mfma_f32_16x16x32_bf16 v[2:5], v[174:177], v[210:213], v[2:5]
	s_setprio 0
	s_barrier
	s_add_u32 s46, s46, 0x100
	s_addc_u32 s47, s47, 0
	s_add_u32 s27, s27, 0x100
	s_addc_u32 s29, s29, 0
	s_cmp_ge_i32 s48, s71
	s_mov_b32 s4, s48
	s_cbranch_scc1 .LBB0_90

.LBB0_113:
	s_andn2_b64 vcc, exec, s[14:15]
	s_cbranch_vccnz .LBB0_116
	s_add_u32 s30, s30, 0x80
	s_addc_u32 s31, s31, 0
	s_add_u32 s19, s34, 0x100
	s_addc_u32 s21, s35, 0
	s_mov_b32 s4, 0
	s_add_i32 s34, s4, 2
	s_add_u32 s35, s30, 0x80
	s_addc_u32 s5, s31, 0
	s_add_i32 s58, 0, 0x10000
	s_cmp_eq_u32 s48, s4
	s_cselect_b32 s5, s27, s5
	s_cselect_b32 s4, s26, s35
	s_cselect_b32 s57, s29, s21
	s_cselect_b32 s56, s28, s19
	s_add_i32 s35, 0, 0x14000
	v_add_u32_e32 v156, s58, v141
	v_add_u32_e32 v172, s35, v141
	ds_read_b128 v[144:147], v156
	ds_read_b128 v[148:151], v156 offset:1024
	ds_read_b128 v[152:155], v156 offset:2048
	ds_read_b128 v[156:159], v156 offset:3072
	ds_read_b128 v[160:163], v172
	ds_read_b128 v[164:167], v172 offset:1024
	ds_read_b128 v[168:171], v172 offset:2048
	ds_read_b128 v[172:175], v172 offset:3072
	v_lshl_add_u64 v[196:197], s[30:31], 0, v[136:137]
	s_add_i32 m0, s3, 0xc000
	ds_read_b128 v[176:179], v143
	ds_read_b128 v[180:183], v143 offset:1024
	ds_read_b128 v[184:187], v143 offset:2048
	ds_read_b128 v[188:191], v143 offset:3072
	ds_read_b128 v[192:195], v143 offset:4096
	ds_read_b128 v[202:205], v143 offset:5120
	ds_read_b128 v[206:209], v143 offset:6144
	ds_read_b128 v[210:213], v143 offset:7168
	global_load_lds_dwordx4 v[196:197], off
	v_lshl_add_u64 v[196:197], s[30:31], 0, v[138:139]
	s_add_i32 m0, s3, 0xe000
	s_nop 0
	global_load_lds_dwordx4 v[196:197], off
	s_waitcnt vmcnt(8)
	s_waitcnt lgkmcnt(0)
	s_barrier
	s_setprio 1
	s_waitcnt lgkmcnt(0)
	v_mfma_f32_16x16x32_bf16 v[122:125], v[144:147], v[176:179], 0
	v_mfma_f32_16x16x32_bf16 v[126:129], v[152:155], v[176:179], 0
	v_mfma_f32_16x16x32_bf16 v[110:113], v[144:147], v[184:187], 0
	v_mfma_f32_16x16x32_bf16 v[106:109], v[152:155], v[184:187], 0
	v_mfma_f32_16x16x32_bf16 v[94:97], v[144:147], v[192:195], 0
	v_mfma_f32_16x16x32_bf16 v[90:93], v[152:155], v[192:195], 0
	v_mfma_f32_16x16x32_bf16 v[78:81], v[144:147], v[206:209], 0
	v_mfma_f32_16x16x32_bf16 v[74:77], v[152:155], v[206:209], 0
	v_mfma_f32_16x16x32_bf16 v[122:125], v[148:151], v[180:183], v[122:125]
	v_mfma_f32_16x16x32_bf16 v[126:129], v[156:159], v[180:183], v[126:129]
	v_mfma_f32_16x16x32_bf16 v[110:113], v[148:151], v[188:191], v[110:113]
	v_mfma_f32_16x16x32_bf16 v[106:109], v[156:159], v[188:191], v[106:109]
	v_mfma_f32_16x16x32_bf16 v[94:97], v[148:151], v[202:205], v[94:97]
	v_mfma_f32_16x16x32_bf16 v[90:93], v[156:159], v[202:205], v[90:93]
	v_mfma_f32_16x16x32_bf16 v[78:81], v[148:151], v[210:213], v[78:81]
	v_mfma_f32_16x16x32_bf16 v[74:77], v[156:159], v[210:213], v[74:77]
	s_setprio 0
	s_setprio 1
	v_mfma_f32_16x16x32_bf16 v[118:121], v[160:163], v[176:179], 0
	v_mfma_f32_16x16x32_bf16 v[114:117], v[168:171], v[176:179], 0
	v_mfma_f32_16x16x32_bf16 v[102:105], v[160:163], v[184:187], 0
	v_mfma_f32_16x16x32_bf16 v[98:101], v[168:171], v[184:187], 0
	v_mfma_f32_16x16x32_bf16 v[86:89], v[160:163], v[192:195], 0
	v_mfma_f32_16x16x32_bf16 v[82:85], v[168:171], v[192:195], 0
	v_mfma_f32_16x16x32_bf16 v[70:73], v[160:163], v[206:209], 0
	v_mfma_f32_16x16x32_bf16 v[66:69], v[168:171], v[206:209], 0
	v_mfma_f32_16x16x32_bf16 v[118:121], v[164:167], v[180:183], v[118:121]
	v_mfma_f32_16x16x32_bf16 v[114:117], v[172:175], v[180:183], v[114:117]
	v_mfma_f32_16x16x32_bf16 v[102:105], v[164:167], v[188:191], v[102:105]
	v_mfma_f32_16x16x32_bf16 v[98:101], v[172:175], v[188:191], v[98:101]
	v_mfma_f32_16x16x32_bf16 v[86:89], v[164:167], v[202:205], v[86:89]
	v_mfma_f32_16x16x32_bf16 v[82:85], v[172:175], v[202:205], v[82:85]
	v_mfma_f32_16x16x32_bf16 v[70:73], v[164:167], v[210:213], v[70:73]
	v_mfma_f32_16x16x32_bf16 v[66:69], v[172:175], v[210:213], v[66:69]
	s_setprio 0
	s_barrier
	s_add_i32 s58, s58, s51
	v_lshl_add_u64 v[196:197], s[56:57], 0, v[0:1]
	s_mov_b32 m0, s58
	ds_read_b128 v[176:179], v143 offset:16384
	ds_read_b128 v[180:183], v143 offset:17408
	ds_read_b128 v[184:187], v143 offset:18432
	ds_read_b128 v[188:191], v143 offset:19456
	ds_read_b128 v[192:195], v143 offset:20480
	ds_read_b128 v[202:205], v143 offset:21504
	ds_read_b128 v[206:209], v143 offset:22528
	ds_read_b128 v[210:213], v143 offset:23552
	global_load_lds_dwordx4 v[196:197], off
	s_add_i32 m0, s58, 0x2000
	v_lshl_add_u64 v[214:215], s[56:57], 0, v[130:131]
	s_add_u32 s56, s56, s8
	s_addc_u32 s57, s57, s9
	s_add_i32 s35, s35, s51
	global_load_lds_dwordx4 v[214:215], off
	v_lshl_add_u64 v[216:217], s[56:57], 0, v[0:1]
	s_mov_b32 m0, s35
	v_lshl_add_u64 v[218:219], s[56:57], 0, v[130:131]
	global_load_lds_dwordx4 v[216:217], off
	s_add_i32 m0, s35, 0x2000
	v_lshl_add_u64 v[220:221], s[4:5], 0, v[132:133]
	global_load_lds_dwordx4 v[218:219], off
	s_mov_b32 m0, s3
	v_lshl_add_u64 v[234:235], s[4:5], 0, v[134:135]
	global_load_lds_dwordx4 v[220:221], off
	s_mov_b32 m0, s42
	s_nop 0
	global_load_lds_dwordx4 v[234:235], off
	s_waitcnt vmcnt(8)
	s_waitcnt lgkmcnt(0)
	s_barrier
	s_setprio 1
	s_waitcnt lgkmcnt(0)
	v_mfma_f32_16x16x32_bf16 v[62:65], v[144:147], v[176:179], 0
	v_mfma_f32_16x16x32_bf16 v[58:61], v[152:155], v[176:179], 0
	v_mfma_f32_16x16x32_bf16 v[46:49], v[144:147], v[184:187], 0
	v_mfma_f32_16x16x32_bf16 v[42:45], v[152:155], v[184:187], 0
	v_mfma_f32_16x16x32_bf16 v[30:33], v[144:147], v[192:195], 0
	v_mfma_f32_16x16x32_bf16 v[26:29], v[152:155], v[192:195], 0
	v_mfma_f32_16x16x32_bf16 v[14:17], v[144:147], v[206:209], 0
	v_mfma_f32_16x16x32_bf16 v[10:13], v[152:155], v[206:209], 0
	v_mfma_f32_16x16x32_bf16 v[62:65], v[148:151], v[180:183], v[62:65]
	v_mfma_f32_16x16x32_bf16 v[58:61], v[156:159], v[180:183], v[58:61]
	v_mfma_f32_16x16x32_bf16 v[46:49], v[148:151], v[188:191], v[46:49]
	v_mfma_f32_16x16x32_bf16 v[42:45], v[156:159], v[188:191], v[42:45]
	v_mfma_f32_16x16x32_bf16 v[30:33], v[148:151], v[202:205], v[30:33]
	v_mfma_f32_16x16x32_bf16 v[26:29], v[156:159], v[202:205], v[26:29]
	v_mfma_f32_16x16x32_bf16 v[14:17], v[148:151], v[210:213], v[14:17]
	v_mfma_f32_16x16x32_bf16 v[10:13], v[156:159], v[210:213], v[10:13]
	s_setprio 0
	s_setprio 1
	v_mfma_f32_16x16x32_bf16 v[54:57], v[160:163], v[176:179], 0
	v_mfma_f32_16x16x32_bf16 v[50:53], v[168:171], v[176:179], 0
	v_mfma_f32_16x16x32_bf16 v[38:41], v[160:163], v[184:187], 0
	v_mfma_f32_16x16x32_bf16 v[34:37], v[168:171], v[184:187], 0
	v_mfma_f32_16x16x32_bf16 v[22:25], v[160:163], v[192:195], 0
	v_mfma_f32_16x16x32_bf16 v[18:21], v[168:171], v[192:195], 0
	v_mfma_f32_16x16x32_bf16 v[6:9], v[160:163], v[206:209], 0
	v_mfma_f32_16x16x32_bf16 v[2:5], v[168:171], v[206:209], 0
	v_mfma_f32_16x16x32_bf16 v[54:57], v[164:167], v[180:183], v[54:57]
	v_mfma_f32_16x16x32_bf16 v[50:53], v[172:175], v[180:183], v[50:53]
	v_mfma_f32_16x16x32_bf16 v[38:41], v[164:167], v[188:191], v[38:41]
	v_mfma_f32_16x16x32_bf16 v[34:37], v[172:175], v[188:191], v[34:37]
	v_mfma_f32_16x16x32_bf16 v[22:25], v[164:167], v[202:205], v[22:25]
	v_mfma_f32_16x16x32_bf16 v[18:21], v[172:175], v[202:205], v[18:21]
	v_mfma_f32_16x16x32_bf16 v[6:9], v[164:167], v[210:213], v[6:9]
	v_mfma_f32_16x16x32_bf16 v[2:5], v[172:175], v[210:213], v[2:5]
	s_setprio 0
	s_barrier
	s_add_i32 s35, 0, 0x18000
	s_add_i32 s56, 0, 0x1c000
	v_add_u32_e32 v156, s35, v141
	v_add_u32_e32 v172, s56, v141
	ds_read_b128 v[144:147], v156
	ds_read_b128 v[148:151], v156 offset:1024
	ds_read_b128 v[152:155], v156 offset:2048
	ds_read_b128 v[156:159], v156 offset:3072
	ds_read_b128 v[160:163], v172
	ds_read_b128 v[164:167], v172 offset:1024
	ds_read_b128 v[168:171], v172 offset:2048
	ds_read_b128 v[172:175], v172 offset:3072
	s_add_u32 s4, s4, s8
	s_addc_u32 s5, s5, s9
	s_mov_b32 m0, s43
	v_lshl_add_u64 v[236:237], s[4:5], 0, v[132:133]
	ds_read_b128 v[176:179], v143 offset:32768
	ds_read_b128 v[180:183], v143 offset:33792
	ds_read_b128 v[184:187], v143 offset:34816
	ds_read_b128 v[188:191], v143 offset:35840
	ds_read_b128 v[192:195], v143 offset:36864
	ds_read_b128 v[202:205], v143 offset:37888
	ds_read_b128 v[206:209], v143 offset:38912
	ds_read_b128 v[210:213], v143 offset:39936
	global_load_lds_dwordx4 v[236:237], off
	v_lshl_add_u64 v[236:237], s[4:5], 0, v[134:135]
	s_mov_b32 m0, s44
	s_nop 0
	global_load_lds_dwordx4 v[236:237], off
	s_waitcnt vmcnt(8)
	s_waitcnt lgkmcnt(0)
	s_barrier
	s_setprio 1
	s_waitcnt lgkmcnt(0)
	v_mfma_f32_16x16x32_bf16 v[122:125], v[144:147], v[176:179], v[122:125]
	v_mfma_f32_16x16x32_bf16 v[126:129], v[152:155], v[176:179], v[126:129]
	v_mfma_f32_16x16x32_bf16 v[110:113], v[144:147], v[184:187], v[110:113]
	v_mfma_f32_16x16x32_bf16 v[106:109], v[152:155], v[184:187], v[106:109]
	v_mfma_f32_16x16x32_bf16 v[94:97], v[144:147], v[192:195], v[94:97]
	v_mfma_f32_16x16x32_bf16 v[90:93], v[152:155], v[192:195], v[90:93]
	v_mfma_f32_16x16x32_bf16 v[78:81], v[144:147], v[206:209], v[78:81]
	v_mfma_f32_16x16x32_bf16 v[74:77], v[152:155], v[206:209], v[74:77]
	v_mfma_f32_16x16x32_bf16 v[122:125], v[148:151], v[180:183], v[122:125]
	v_mfma_f32_16x16x32_bf16 v[126:129], v[156:159], v[180:183], v[126:129]
	v_mfma_f32_16x16x32_bf16 v[110:113], v[148:151], v[188:191], v[110:113]
	v_mfma_f32_16x16x32_bf16 v[106:109], v[156:159], v[188:191], v[106:109]
	v_mfma_f32_16x16x32_bf16 v[94:97], v[148:151], v[202:205], v[94:97]
	v_mfma_f32_16x16x32_bf16 v[90:93], v[156:159], v[202:205], v[90:93]
	v_mfma_f32_16x16x32_bf16 v[78:81], v[148:151], v[210:213], v[78:81]
	v_mfma_f32_16x16x32_bf16 v[74:77], v[156:159], v[210:213], v[74:77]
	s_setprio 0
	s_setprio 1
	v_mfma_f32_16x16x32_bf16 v[118:121], v[160:163], v[176:179], v[118:121]
	v_mfma_f32_16x16x32_bf16 v[114:117], v[168:171], v[176:179], v[114:117]
	v_mfma_f32_16x16x32_bf16 v[102:105], v[160:163], v[184:187], v[102:105]
	v_mfma_f32_16x16x32_bf16 v[98:101], v[168:171], v[184:187], v[98:101]
	v_mfma_f32_16x16x32_bf16 v[86:89], v[160:163], v[192:195], v[86:89]
	v_mfma_f32_16x16x32_bf16 v[82:85], v[168:171], v[192:195], v[82:85]
	v_mfma_f32_16x16x32_bf16 v[70:73], v[160:163], v[206:209], v[70:73]
	v_mfma_f32_16x16x32_bf16 v[66:69], v[168:171], v[206:209], v[66:69]
	v_mfma_f32_16x16x32_bf16 v[118:121], v[164:167], v[180:183], v[118:121]
	v_mfma_f32_16x16x32_bf16 v[114:117], v[172:175], v[180:183], v[114:117]
	v_mfma_f32_16x16x32_bf16 v[102:105], v[164:167], v[188:191], v[102:105]
	v_mfma_f32_16x16x32_bf16 v[98:101], v[172:175], v[188:191], v[98:101]
	v_mfma_f32_16x16x32_bf16 v[86:89], v[164:167], v[202:205], v[86:89]
	v_mfma_f32_16x16x32_bf16 v[82:85], v[172:175], v[202:205], v[82:85]
	v_mfma_f32_16x16x32_bf16 v[70:73], v[164:167], v[210:213], v[70:73]
	v_mfma_f32_16x16x32_bf16 v[66:69], v[172:175], v[210:213], v[66:69]
	s_setprio 0
	s_barrier
	s_add_i32 s4, s35, s51
	v_lshl_add_u64 v[196:197], v[196:197], 0, s[94:95]
	s_mov_b32 m0, s4
	ds_read_b128 v[176:179], v143 offset:49152
	ds_read_b128 v[180:183], v143 offset:50176
	ds_read_b128 v[184:187], v143 offset:51200
	ds_read_b128 v[188:191], v143 offset:52224
	ds_read_b128 v[192:195], v143 offset:53248
	ds_read_b128 v[202:205], v143 offset:54272
	ds_read_b128 v[206:209], v143 offset:55296
	ds_read_b128 v[210:213], v143 offset:56320
	global_load_lds_dwordx4 v[196:197], off
	v_lshl_add_u64 v[196:197], v[214:215], 0, s[94:95]
	s_add_i32 m0, s4, 0x2000
	s_add_i32 s4, s56, s51
	global_load_lds_dwordx4 v[196:197], off
	v_lshl_add_u64 v[196:197], v[216:217], 0, s[94:95]
	s_mov_b32 m0, s4
	s_nop 0
	global_load_lds_dwordx4 v[196:197], off
	v_lshl_add_u64 v[196:197], v[218:219], 0, s[94:95]
	s_add_i32 m0, s4, 0x2000
	s_nop 0
	global_load_lds_dwordx4 v[196:197], off
	v_lshl_add_u64 v[196:197], v[220:221], 0, s[94:95]
	s_mov_b32 m0, s46
	s_nop 0
	global_load_lds_dwordx4 v[196:197], off
	v_lshl_add_u64 v[196:197], v[234:235], 0, s[94:95]
	s_mov_b32 m0, s47
	s_nop 0
	global_load_lds_dwordx4 v[196:197], off
	s_waitcnt vmcnt(8)
	s_waitcnt lgkmcnt(0)
	s_barrier
	s_setprio 1
	s_waitcnt lgkmcnt(0)
	v_mfma_f32_16x16x32_bf16 v[62:65], v[144:147], v[176:179], v[62:65]
	v_mfma_f32_16x16x32_bf16 v[58:61], v[152:155], v[176:179], v[58:61]
	v_mfma_f32_16x16x32_bf16 v[46:49], v[144:147], v[184:187], v[46:49]
	v_mfma_f32_16x16x32_bf16 v[42:45], v[152:155], v[184:187], v[42:45]
	v_mfma_f32_16x16x32_bf16 v[30:33], v[144:147], v[192:195], v[30:33]
	v_mfma_f32_16x16x32_bf16 v[26:29], v[152:155], v[192:195], v[26:29]
	v_mfma_f32_16x16x32_bf16 v[14:17], v[144:147], v[206:209], v[14:17]
	v_mfma_f32_16x16x32_bf16 v[10:13], v[152:155], v[206:209], v[10:13]
	v_mfma_f32_16x16x32_bf16 v[62:65], v[148:151], v[180:183], v[62:65]
	v_mfma_f32_16x16x32_bf16 v[58:61], v[156:159], v[180:183], v[58:61]
	v_mfma_f32_16x16x32_bf16 v[46:49], v[148:151], v[188:191], v[46:49]
	v_mfma_f32_16x16x32_bf16 v[42:45], v[156:159], v[188:191], v[42:45]
	v_mfma_f32_16x16x32_bf16 v[30:33], v[148:151], v[202:205], v[30:33]
	v_mfma_f32_16x16x32_bf16 v[26:29], v[156:159], v[202:205], v[26:29]
	v_mfma_f32_16x16x32_bf16 v[14:17], v[148:151], v[210:213], v[14:17]
	v_mfma_f32_16x16x32_bf16 v[10:13], v[156:159], v[210:213], v[10:13]
	s_setprio 0
	s_setprio 1
	v_mfma_f32_16x16x32_bf16 v[54:57], v[160:163], v[176:179], v[54:57]
	v_mfma_f32_16x16x32_bf16 v[50:53], v[168:171], v[176:179], v[50:53]
	v_mfma_f32_16x16x32_bf16 v[38:41], v[160:163], v[184:187], v[38:41]
	v_mfma_f32_16x16x32_bf16 v[34:37], v[168:171], v[184:187], v[34:37]
	v_mfma_f32_16x16x32_bf16 v[22:25], v[160:163], v[192:195], v[22:25]
	v_mfma_f32_16x16x32_bf16 v[18:21], v[168:171], v[192:195], v[18:21]
	v_mfma_f32_16x16x32_bf16 v[6:9], v[160:163], v[206:209], v[6:9]
	v_mfma_f32_16x16x32_bf16 v[2:5], v[168:171], v[206:209], v[2:5]
	v_mfma_f32_16x16x32_bf16 v[54:57], v[164:167], v[180:183], v[54:57]
	v_mfma_f32_16x16x32_bf16 v[50:53], v[172:175], v[180:183], v[50:53]
	v_mfma_f32_16x16x32_bf16 v[38:41], v[164:167], v[188:191], v[38:41]
	v_mfma_f32_16x16x32_bf16 v[34:37], v[172:175], v[188:191], v[34:37]
	v_mfma_f32_16x16x32_bf16 v[22:25], v[164:167], v[202:205], v[22:25]
	v_mfma_f32_16x16x32_bf16 v[18:21], v[172:175], v[202:205], v[18:21]
	v_mfma_f32_16x16x32_bf16 v[6:9], v[164:167], v[210:213], v[6:9]
	v_mfma_f32_16x16x32_bf16 v[2:5], v[172:175], v[210:213], v[2:5]
	s_setprio 0
	s_barrier
	s_add_u32 s30, s30, 0x100
	s_addc_u32 s31, s31, 0
	s_add_u32 s19, s19, 0x100
	s_addc_u32 s21, s21, 0
	s_cmp_ge_i32 s34, s45
	s_mov_b32 s4, s34
	s_cbranch_scc1 .LBB0_116

.LBB0_542:
	s_andn2_b64 vcc, exec, s[14:15]
	s_cbranch_vccnz .LBB0_546
	s_add_u32 s30, s30, 0x80
	s_addc_u32 s31, s31, 0
	s_add_u32 s19, s34, 0x100
	s_addc_u32 s21, s35, 0
	s_mov_b32 s4, 0
	s_add_i32 s34, s4, 2
	s_add_u32 s35, s30, 0x80
	s_addc_u32 s5, s31, 0
	s_add_i32 s51, 0, 0x10000
	s_cmp_eq_u32 s47, s4
	s_cselect_b32 s5, s27, s5
	s_cselect_b32 s4, s26, s35
	s_cselect_b32 s57, s29, s21
	s_cselect_b32 s56, s28, s19
	s_add_i32 s35, 0, 0x14000
	v_add_u32_e32 v156, s51, v141
	v_add_u32_e32 v172, s35, v141
	ds_read_b128 v[144:147], v156
	ds_read_b128 v[148:151], v156 offset:1024
	ds_read_b128 v[152:155], v156 offset:2048
	ds_read_b128 v[156:159], v156 offset:3072
	ds_read_b128 v[160:163], v172
	ds_read_b128 v[164:167], v172 offset:1024
	ds_read_b128 v[168:171], v172 offset:2048
	ds_read_b128 v[172:175], v172 offset:3072
	v_lshl_add_u64 v[196:197], s[30:31], 0, v[136:137]
	s_add_i32 m0, s40, 0xc000
	ds_read_b128 v[176:179], v143
	ds_read_b128 v[180:183], v143 offset:1024
	ds_read_b128 v[184:187], v143 offset:2048
	ds_read_b128 v[188:191], v143 offset:3072
	ds_read_b128 v[192:195], v143 offset:4096
	ds_read_b128 v[202:205], v143 offset:5120
	ds_read_b128 v[206:209], v143 offset:6144
	ds_read_b128 v[210:213], v143 offset:7168
	global_load_lds_dwordx4 v[196:197], off
	v_lshl_add_u64 v[196:197], s[30:31], 0, v[138:139]
	s_add_i32 m0, s40, 0xe000
	s_nop 0
	global_load_lds_dwordx4 v[196:197], off
	s_waitcnt vmcnt(8)
	s_waitcnt lgkmcnt(0)
	s_barrier
	s_setprio 1
	s_waitcnt lgkmcnt(0)
	v_mfma_f32_16x16x32_bf16 v[122:125], v[144:147], v[176:179], 0
	v_mfma_f32_16x16x32_bf16 v[126:129], v[152:155], v[176:179], 0
	v_mfma_f32_16x16x32_bf16 v[110:113], v[144:147], v[184:187], 0
	v_mfma_f32_16x16x32_bf16 v[106:109], v[152:155], v[184:187], 0
	v_mfma_f32_16x16x32_bf16 v[94:97], v[144:147], v[192:195], 0
	v_mfma_f32_16x16x32_bf16 v[90:93], v[152:155], v[192:195], 0
	v_mfma_f32_16x16x32_bf16 v[78:81], v[144:147], v[206:209], 0
	v_mfma_f32_16x16x32_bf16 v[74:77], v[152:155], v[206:209], 0
	v_mfma_f32_16x16x32_bf16 v[122:125], v[148:151], v[180:183], v[122:125]
	v_mfma_f32_16x16x32_bf16 v[126:129], v[156:159], v[180:183], v[126:129]
	v_mfma_f32_16x16x32_bf16 v[110:113], v[148:151], v[188:191], v[110:113]
	v_mfma_f32_16x16x32_bf16 v[106:109], v[156:159], v[188:191], v[106:109]
	v_mfma_f32_16x16x32_bf16 v[94:97], v[148:151], v[202:205], v[94:97]
	v_mfma_f32_16x16x32_bf16 v[90:93], v[156:159], v[202:205], v[90:93]
	v_mfma_f32_16x16x32_bf16 v[78:81], v[148:151], v[210:213], v[78:81]
	v_mfma_f32_16x16x32_bf16 v[74:77], v[156:159], v[210:213], v[74:77]
	s_setprio 0
	s_setprio 1
	v_mfma_f32_16x16x32_bf16 v[118:121], v[160:163], v[176:179], 0
	v_mfma_f32_16x16x32_bf16 v[114:117], v[168:171], v[176:179], 0
	v_mfma_f32_16x16x32_bf16 v[102:105], v[160:163], v[184:187], 0
	v_mfma_f32_16x16x32_bf16 v[98:101], v[168:171], v[184:187], 0
	v_mfma_f32_16x16x32_bf16 v[86:89], v[160:163], v[192:195], 0
	v_mfma_f32_16x16x32_bf16 v[82:85], v[168:171], v[192:195], 0
	v_mfma_f32_16x16x32_bf16 v[70:73], v[160:163], v[206:209], 0
	v_mfma_f32_16x16x32_bf16 v[66:69], v[168:171], v[206:209], 0
	v_mfma_f32_16x16x32_bf16 v[118:121], v[164:167], v[180:183], v[118:121]
	v_mfma_f32_16x16x32_bf16 v[114:117], v[172:175], v[180:183], v[114:117]
	v_mfma_f32_16x16x32_bf16 v[102:105], v[164:167], v[188:191], v[102:105]
	v_mfma_f32_16x16x32_bf16 v[98:101], v[172:175], v[188:191], v[98:101]
	v_mfma_f32_16x16x32_bf16 v[86:89], v[164:167], v[202:205], v[86:89]
	v_mfma_f32_16x16x32_bf16 v[82:85], v[172:175], v[202:205], v[82:85]
	v_mfma_f32_16x16x32_bf16 v[70:73], v[164:167], v[210:213], v[70:73]
	v_mfma_f32_16x16x32_bf16 v[66:69], v[172:175], v[210:213], v[66:69]
	s_setprio 0
	s_barrier
	s_add_i32 s51, s51, s39
	v_lshl_add_u64 v[196:197], s[56:57], 0, v[0:1]
	s_mov_b32 m0, s51
	ds_read_b128 v[176:179], v143 offset:16384
	ds_read_b128 v[180:183], v143 offset:17408
	ds_read_b128 v[184:187], v143 offset:18432
	ds_read_b128 v[188:191], v143 offset:19456
	ds_read_b128 v[192:195], v143 offset:20480
	ds_read_b128 v[202:205], v143 offset:21504
	ds_read_b128 v[206:209], v143 offset:22528
	ds_read_b128 v[210:213], v143 offset:23552
	global_load_lds_dwordx4 v[196:197], off
	s_add_i32 m0, s51, 0x2000
	v_lshl_add_u64 v[214:215], s[56:57], 0, v[130:131]
	s_add_u32 s56, s56, s8
	s_addc_u32 s57, s57, s9
	s_add_i32 s35, s35, s39
	global_load_lds_dwordx4 v[214:215], off
	v_lshl_add_u64 v[216:217], s[56:57], 0, v[0:1]
	s_mov_b32 m0, s35
	v_lshl_add_u64 v[218:219], s[56:57], 0, v[130:131]
	global_load_lds_dwordx4 v[216:217], off
	s_add_i32 m0, s35, 0x2000
	v_lshl_add_u64 v[220:221], s[4:5], 0, v[132:133]
	global_load_lds_dwordx4 v[218:219], off
	s_mov_b32 m0, s40
	v_lshl_add_u64 v[234:235], s[4:5], 0, v[134:135]
	global_load_lds_dwordx4 v[220:221], off
	s_mov_b32 m0, s41
	s_nop 0
	global_load_lds_dwordx4 v[234:235], off
	s_waitcnt vmcnt(8)
	s_waitcnt lgkmcnt(0)
	s_barrier
	s_setprio 1
	s_waitcnt lgkmcnt(0)
	v_mfma_f32_16x16x32_bf16 v[62:65], v[144:147], v[176:179], 0
	v_mfma_f32_16x16x32_bf16 v[58:61], v[152:155], v[176:179], 0
	v_mfma_f32_16x16x32_bf16 v[46:49], v[144:147], v[184:187], 0
	v_mfma_f32_16x16x32_bf16 v[42:45], v[152:155], v[184:187], 0
	v_mfma_f32_16x16x32_bf16 v[30:33], v[144:147], v[192:195], 0
	v_mfma_f32_16x16x32_bf16 v[26:29], v[152:155], v[192:195], 0
	v_mfma_f32_16x16x32_bf16 v[14:17], v[144:147], v[206:209], 0
	v_mfma_f32_16x16x32_bf16 v[10:13], v[152:155], v[206:209], 0
	v_mfma_f32_16x16x32_bf16 v[62:65], v[148:151], v[180:183], v[62:65]
	v_mfma_f32_16x16x32_bf16 v[58:61], v[156:159], v[180:183], v[58:61]
	v_mfma_f32_16x16x32_bf16 v[46:49], v[148:151], v[188:191], v[46:49]
	v_mfma_f32_16x16x32_bf16 v[42:45], v[156:159], v[188:191], v[42:45]
	v_mfma_f32_16x16x32_bf16 v[30:33], v[148:151], v[202:205], v[30:33]
	v_mfma_f32_16x16x32_bf16 v[26:29], v[156:159], v[202:205], v[26:29]
	v_mfma_f32_16x16x32_bf16 v[14:17], v[148:151], v[210:213], v[14:17]
	v_mfma_f32_16x16x32_bf16 v[10:13], v[156:159], v[210:213], v[10:13]
	s_setprio 0
	s_setprio 1
	v_mfma_f32_16x16x32_bf16 v[54:57], v[160:163], v[176:179], 0
	v_mfma_f32_16x16x32_bf16 v[50:53], v[168:171], v[176:179], 0
	v_mfma_f32_16x16x32_bf16 v[38:41], v[160:163], v[184:187], 0
	v_mfma_f32_16x16x32_bf16 v[34:37], v[168:171], v[184:187], 0
	v_mfma_f32_16x16x32_bf16 v[22:25], v[160:163], v[192:195], 0
	v_mfma_f32_16x16x32_bf16 v[18:21], v[168:171], v[192:195], 0
	v_mfma_f32_16x16x32_bf16 v[6:9], v[160:163], v[206:209], 0
	v_mfma_f32_16x16x32_bf16 v[2:5], v[168:171], v[206:209], 0
	v_mfma_f32_16x16x32_bf16 v[54:57], v[164:167], v[180:183], v[54:57]
	v_mfma_f32_16x16x32_bf16 v[50:53], v[172:175], v[180:183], v[50:53]
	v_mfma_f32_16x16x32_bf16 v[38:41], v[164:167], v[188:191], v[38:41]
	v_mfma_f32_16x16x32_bf16 v[34:37], v[172:175], v[188:191], v[34:37]
	v_mfma_f32_16x16x32_bf16 v[22:25], v[164:167], v[202:205], v[22:25]
	v_mfma_f32_16x16x32_bf16 v[18:21], v[172:175], v[202:205], v[18:21]
	v_mfma_f32_16x16x32_bf16 v[6:9], v[164:167], v[210:213], v[6:9]
	v_mfma_f32_16x16x32_bf16 v[2:5], v[172:175], v[210:213], v[2:5]
	s_setprio 0
	s_barrier
	s_add_i32 s35, 0, 0x18000
	s_add_i32 s51, 0, 0x1c000
	v_add_u32_e32 v156, s35, v141
	v_add_u32_e32 v172, s51, v141
	ds_read_b128 v[144:147], v156
	ds_read_b128 v[148:151], v156 offset:1024
	ds_read_b128 v[152:155], v156 offset:2048
	ds_read_b128 v[156:159], v156 offset:3072
	ds_read_b128 v[160:163], v172
	ds_read_b128 v[164:167], v172 offset:1024
	ds_read_b128 v[168:171], v172 offset:2048
	ds_read_b128 v[172:175], v172 offset:3072
	s_add_u32 s4, s4, s8
	s_addc_u32 s5, s5, s9
	s_mov_b32 m0, s42
	v_lshl_add_u64 v[236:237], s[4:5], 0, v[132:133]
	ds_read_b128 v[176:179], v143 offset:32768
	ds_read_b128 v[180:183], v143 offset:33792
	ds_read_b128 v[184:187], v143 offset:34816
	ds_read_b128 v[188:191], v143 offset:35840
	ds_read_b128 v[192:195], v143 offset:36864
	ds_read_b128 v[202:205], v143 offset:37888
	ds_read_b128 v[206:209], v143 offset:38912
	ds_read_b128 v[210:213], v143 offset:39936
	global_load_lds_dwordx4 v[236:237], off
	v_lshl_add_u64 v[236:237], s[4:5], 0, v[134:135]
	s_mov_b32 m0, s43
	s_nop 0
	global_load_lds_dwordx4 v[236:237], off
	s_waitcnt vmcnt(8)
	s_waitcnt lgkmcnt(0)
	s_barrier
	s_setprio 1
	s_waitcnt lgkmcnt(0)
	v_mfma_f32_16x16x32_bf16 v[122:125], v[144:147], v[176:179], v[122:125]
	v_mfma_f32_16x16x32_bf16 v[126:129], v[152:155], v[176:179], v[126:129]
	v_mfma_f32_16x16x32_bf16 v[110:113], v[144:147], v[184:187], v[110:113]
	v_mfma_f32_16x16x32_bf16 v[106:109], v[152:155], v[184:187], v[106:109]
	v_mfma_f32_16x16x32_bf16 v[94:97], v[144:147], v[192:195], v[94:97]
	v_mfma_f32_16x16x32_bf16 v[90:93], v[152:155], v[192:195], v[90:93]
	v_mfma_f32_16x16x32_bf16 v[78:81], v[144:147], v[206:209], v[78:81]
	v_mfma_f32_16x16x32_bf16 v[74:77], v[152:155], v[206:209], v[74:77]
	v_mfma_f32_16x16x32_bf16 v[122:125], v[148:151], v[180:183], v[122:125]
	v_mfma_f32_16x16x32_bf16 v[126:129], v[156:159], v[180:183], v[126:129]
	v_mfma_f32_16x16x32_bf16 v[110:113], v[148:151], v[188:191], v[110:113]
	v_mfma_f32_16x16x32_bf16 v[106:109], v[156:159], v[188:191], v[106:109]
	v_mfma_f32_16x16x32_bf16 v[94:97], v[148:151], v[202:205], v[94:97]
	v_mfma_f32_16x16x32_bf16 v[90:93], v[156:159], v[202:205], v[90:93]
	v_mfma_f32_16x16x32_bf16 v[78:81], v[148:151], v[210:213], v[78:81]
	v_mfma_f32_16x16x32_bf16 v[74:77], v[156:159], v[210:213], v[74:77]
	s_setprio 0
	s_setprio 1
	v_mfma_f32_16x16x32_bf16 v[118:121], v[160:163], v[176:179], v[118:121]
	v_mfma_f32_16x16x32_bf16 v[114:117], v[168:171], v[176:179], v[114:117]
	v_mfma_f32_16x16x32_bf16 v[102:105], v[160:163], v[184:187], v[102:105]
	v_mfma_f32_16x16x32_bf16 v[98:101], v[168:171], v[184:187], v[98:101]
	v_mfma_f32_16x16x32_bf16 v[86:89], v[160:163], v[192:195], v[86:89]
	v_mfma_f32_16x16x32_bf16 v[82:85], v[168:171], v[192:195], v[82:85]
	v_mfma_f32_16x16x32_bf16 v[70:73], v[160:163], v[206:209], v[70:73]
	v_mfma_f32_16x16x32_bf16 v[66:69], v[168:171], v[206:209], v[66:69]
	v_mfma_f32_16x16x32_bf16 v[118:121], v[164:167], v[180:183], v[118:121]
	v_mfma_f32_16x16x32_bf16 v[114:117], v[172:175], v[180:183], v[114:117]
	v_mfma_f32_16x16x32_bf16 v[102:105], v[164:167], v[188:191], v[102:105]
	v_mfma_f32_16x16x32_bf16 v[98:101], v[172:175], v[188:191], v[98:101]
	v_mfma_f32_16x16x32_bf16 v[86:89], v[164:167], v[202:205], v[86:89]
	v_mfma_f32_16x16x32_bf16 v[82:85], v[172:175], v[202:205], v[82:85]
	v_mfma_f32_16x16x32_bf16 v[70:73], v[164:167], v[210:213], v[70:73]
	v_mfma_f32_16x16x32_bf16 v[66:69], v[172:175], v[210:213], v[66:69]
	s_setprio 0
	s_barrier
	s_add_i32 s4, s35, s39
	v_lshl_add_u64 v[196:197], v[196:197], 0, s[94:95]
	s_mov_b32 m0, s4
	ds_read_b128 v[176:179], v143 offset:49152
	ds_read_b128 v[180:183], v143 offset:50176
	ds_read_b128 v[184:187], v143 offset:51200
	ds_read_b128 v[188:191], v143 offset:52224
	ds_read_b128 v[192:195], v143 offset:53248
	ds_read_b128 v[202:205], v143 offset:54272
	ds_read_b128 v[206:209], v143 offset:55296
	ds_read_b128 v[210:213], v143 offset:56320
	global_load_lds_dwordx4 v[196:197], off
	v_lshl_add_u64 v[196:197], v[214:215], 0, s[94:95]
	s_add_i32 m0, s4, 0x2000
	s_add_i32 s4, s51, s39
	global_load_lds_dwordx4 v[196:197], off
	v_lshl_add_u64 v[196:197], v[216:217], 0, s[94:95]
	s_mov_b32 m0, s4
	s_nop 0
	global_load_lds_dwordx4 v[196:197], off
	v_lshl_add_u64 v[196:197], v[218:219], 0, s[94:95]
	s_add_i32 m0, s4, 0x2000
	s_nop 0
	global_load_lds_dwordx4 v[196:197], off
	v_lshl_add_u64 v[196:197], v[220:221], 0, s[94:95]
	s_mov_b32 m0, s45
	s_nop 0
	global_load_lds_dwordx4 v[196:197], off
	v_lshl_add_u64 v[196:197], v[234:235], 0, s[94:95]
	s_mov_b32 m0, s46
	s_nop 0
	global_load_lds_dwordx4 v[196:197], off
	s_waitcnt vmcnt(8)
	s_waitcnt lgkmcnt(0)
	s_barrier
	s_setprio 1
	s_waitcnt lgkmcnt(0)
	v_mfma_f32_16x16x32_bf16 v[62:65], v[144:147], v[176:179], v[62:65]
	v_mfma_f32_16x16x32_bf16 v[58:61], v[152:155], v[176:179], v[58:61]
	v_mfma_f32_16x16x32_bf16 v[46:49], v[144:147], v[184:187], v[46:49]
	v_mfma_f32_16x16x32_bf16 v[42:45], v[152:155], v[184:187], v[42:45]
	v_mfma_f32_16x16x32_bf16 v[30:33], v[144:147], v[192:195], v[30:33]
	v_mfma_f32_16x16x32_bf16 v[26:29], v[152:155], v[192:195], v[26:29]
	v_mfma_f32_16x16x32_bf16 v[14:17], v[144:147], v[206:209], v[14:17]
	v_mfma_f32_16x16x32_bf16 v[10:13], v[152:155], v[206:209], v[10:13]
	v_mfma_f32_16x16x32_bf16 v[62:65], v[148:151], v[180:183], v[62:65]
	v_mfma_f32_16x16x32_bf16 v[58:61], v[156:159], v[180:183], v[58:61]
	v_mfma_f32_16x16x32_bf16 v[46:49], v[148:151], v[188:191], v[46:49]
	v_mfma_f32_16x16x32_bf16 v[42:45], v[156:159], v[188:191], v[42:45]
	v_mfma_f32_16x16x32_bf16 v[30:33], v[148:151], v[202:205], v[30:33]
	v_mfma_f32_16x16x32_bf16 v[26:29], v[156:159], v[202:205], v[26:29]
	v_mfma_f32_16x16x32_bf16 v[14:17], v[148:151], v[210:213], v[14:17]
	v_mfma_f32_16x16x32_bf16 v[10:13], v[156:159], v[210:213], v[10:13]
	s_setprio 0
	s_setprio 1
	v_mfma_f32_16x16x32_bf16 v[54:57], v[160:163], v[176:179], v[54:57]
	v_mfma_f32_16x16x32_bf16 v[50:53], v[168:171], v[176:179], v[50:53]
	v_mfma_f32_16x16x32_bf16 v[38:41], v[160:163], v[184:187], v[38:41]
	v_mfma_f32_16x16x32_bf16 v[34:37], v[168:171], v[184:187], v[34:37]
	v_mfma_f32_16x16x32_bf16 v[22:25], v[160:163], v[192:195], v[22:25]
	v_mfma_f32_16x16x32_bf16 v[18:21], v[168:171], v[192:195], v[18:21]
	v_mfma_f32_16x16x32_bf16 v[6:9], v[160:163], v[206:209], v[6:9]
	v_mfma_f32_16x16x32_bf16 v[2:5], v[168:171], v[206:209], v[2:5]
	v_mfma_f32_16x16x32_bf16 v[54:57], v[164:167], v[180:183], v[54:57]
	v_mfma_f32_16x16x32_bf16 v[50:53], v[172:175], v[180:183], v[50:53]
	v_mfma_f32_16x16x32_bf16 v[38:41], v[164:167], v[188:191], v[38:41]
	v_mfma_f32_16x16x32_bf16 v[34:37], v[172:175], v[188:191], v[34:37]
	v_mfma_f32_16x16x32_bf16 v[22:25], v[164:167], v[202:205], v[22:25]
	v_mfma_f32_16x16x32_bf16 v[18:21], v[172:175], v[202:205], v[18:21]
	v_mfma_f32_16x16x32_bf16 v[6:9], v[164:167], v[210:213], v[6:9]
	v_mfma_f32_16x16x32_bf16 v[2:5], v[172:175], v[210:213], v[2:5]
	s_setprio 0
	s_barrier
	s_add_u32 s30, s30, 0x100
	s_addc_u32 s31, s31, 0
	s_add_u32 s19, s19, 0x100
	s_addc_u32 s21, s21, 0
	s_cmp_ge_i32 s34, s44
	s_mov_b32 s4, s34
	s_cbranch_scc1 .Lpeel_exit_2
.LBB0_544:
	s_add_i32 s34, s4, 2
	s_add_u32 s35, s30, 0x80
	s_addc_u32 s5, s31, 0
	s_add_i32 s51, 0, 0x10000
	s_cmp_eq_u32 s47, s4
	s_cselect_b32 s5, s27, s5
	s_cselect_b32 s4, s26, s35
	s_cselect_b32 s57, s29, s21
	s_cselect_b32 s56, s28, s19
	s_add_i32 s35, 0, 0x14000
	v_add_u32_e32 v156, s51, v141
	v_add_u32_e32 v172, s35, v141
	ds_read_b128 v[144:147], v156
	ds_read_b128 v[148:151], v156 offset:1024
	ds_read_b128 v[152:155], v156 offset:2048
	ds_read_b128 v[156:159], v156 offset:3072
	ds_read_b128 v[160:163], v172
	ds_read_b128 v[164:167], v172 offset:1024
	ds_read_b128 v[168:171], v172 offset:2048
	ds_read_b128 v[172:175], v172 offset:3072
	v_lshl_add_u64 v[196:197], s[30:31], 0, v[136:137]
	s_add_i32 m0, s40, 0xc000
	ds_read_b128 v[176:179], v143
	ds_read_b128 v[180:183], v143 offset:1024
	ds_read_b128 v[184:187], v143 offset:2048
	ds_read_b128 v[188:191], v143 offset:3072
	ds_read_b128 v[192:195], v143 offset:4096
	ds_read_b128 v[202:205], v143 offset:5120
	ds_read_b128 v[206:209], v143 offset:6144
	ds_read_b128 v[210:213], v143 offset:7168
	global_load_lds_dwordx4 v[196:197], off
	v_lshl_add_u64 v[196:197], s[30:31], 0, v[138:139]
	s_add_i32 m0, s40, 0xe000
	s_nop 0
	global_load_lds_dwordx4 v[196:197], off
	s_waitcnt vmcnt(8)
	s_waitcnt lgkmcnt(0)
	s_barrier
	s_setprio 1
	s_waitcnt lgkmcnt(0)
	v_mfma_f32_16x16x32_bf16 v[122:125], v[144:147], v[176:179], v[122:125]
	v_mfma_f32_16x16x32_bf16 v[126:129], v[152:155], v[176:179], v[126:129]
	v_mfma_f32_16x16x32_bf16 v[110:113], v[144:147], v[184:187], v[110:113]
	v_mfma_f32_16x16x32_bf16 v[106:109], v[152:155], v[184:187], v[106:109]
	v_mfma_f32_16x16x32_bf16 v[94:97], v[144:147], v[192:195], v[94:97]
	v_mfma_f32_16x16x32_bf16 v[90:93], v[152:155], v[192:195], v[90:93]
	v_mfma_f32_16x16x32_bf16 v[78:81], v[144:147], v[206:209], v[78:81]
	v_mfma_f32_16x16x32_bf16 v[74:77], v[152:155], v[206:209], v[74:77]
	v_mfma_f32_16x16x32_bf16 v[122:125], v[148:151], v[180:183], v[122:125]
	v_mfma_f32_16x16x32_bf16 v[126:129], v[156:159], v[180:183], v[126:129]
	v_mfma_f32_16x16x32_bf16 v[110:113], v[148:151], v[188:191], v[110:113]
	v_mfma_f32_16x16x32_bf16 v[106:109], v[156:159], v[188:191], v[106:109]
	v_mfma_f32_16x16x32_bf16 v[94:97], v[148:151], v[202:205], v[94:97]
	v_mfma_f32_16x16x32_bf16 v[90:93], v[156:159], v[202:205], v[90:93]
	v_mfma_f32_16x16x32_bf16 v[78:81], v[148:151], v[210:213], v[78:81]
	v_mfma_f32_16x16x32_bf16 v[74:77], v[156:159], v[210:213], v[74:77]
	s_setprio 0
	s_setprio 1
	v_mfma_f32_16x16x32_bf16 v[118:121], v[160:163], v[176:179], v[118:121]
	v_mfma_f32_16x16x32_bf16 v[114:117], v[168:171], v[176:179], v[114:117]
	v_mfma_f32_16x16x32_bf16 v[102:105], v[160:163], v[184:187], v[102:105]
	v_mfma_f32_16x16x32_bf16 v[98:101], v[168:171], v[184:187], v[98:101]
	v_mfma_f32_16x16x32_bf16 v[86:89], v[160:163], v[192:195], v[86:89]
	v_mfma_f32_16x16x32_bf16 v[82:85], v[168:171], v[192:195], v[82:85]
	v_mfma_f32_16x16x32_bf16 v[70:73], v[160:163], v[206:209], v[70:73]
	v_mfma_f32_16x16x32_bf16 v[66:69], v[168:171], v[206:209], v[66:69]
	v_mfma_f32_16x16x32_bf16 v[118:121], v[164:167], v[180:183], v[118:121]
	v_mfma_f32_16x16x32_bf16 v[114:117], v[172:175], v[180:183], v[114:117]
	v_mfma_f32_16x16x32_bf16 v[102:105], v[164:167], v[188:191], v[102:105]
	v_mfma_f32_16x16x32_bf16 v[98:101], v[172:175], v[188:191], v[98:101]
	v_mfma_f32_16x16x32_bf16 v[86:89], v[164:167], v[202:205], v[86:89]
	v_mfma_f32_16x16x32_bf16 v[82:85], v[172:175], v[202:205], v[82:85]
	v_mfma_f32_16x16x32_bf16 v[70:73], v[164:167], v[210:213], v[70:73]
	v_mfma_f32_16x16x32_bf16 v[66:69], v[172:175], v[210:213], v[66:69]
	s_setprio 0
	s_barrier
	s_add_i32 s51, s51, s39
	v_lshl_add_u64 v[196:197], s[56:57], 0, v[0:1]
	s_mov_b32 m0, s51
	ds_read_b128 v[176:179], v143 offset:16384
	ds_read_b128 v[180:183], v143 offset:17408
	ds_read_b128 v[184:187], v143 offset:18432
	ds_read_b128 v[188:191], v143 offset:19456
	ds_read_b128 v[192:195], v143 offset:20480
	ds_read_b128 v[202:205], v143 offset:21504
	ds_read_b128 v[206:209], v143 offset:22528
	ds_read_b128 v[210:213], v143 offset:23552
	global_load_lds_dwordx4 v[196:197], off
	s_add_i32 m0, s51, 0x2000
	v_lshl_add_u64 v[214:215], s[56:57], 0, v[130:131]
	s_add_u32 s56, s56, s8
	s_addc_u32 s57, s57, s9
	s_add_i32 s35, s35, s39
	global_load_lds_dwordx4 v[214:215], off
	v_lshl_add_u64 v[216:217], s[56:57], 0, v[0:1]
	s_mov_b32 m0, s35
	v_lshl_add_u64 v[218:219], s[56:57], 0, v[130:131]
	global_load_lds_dwordx4 v[216:217], off
	s_add_i32 m0, s35, 0x2000
	v_lshl_add_u64 v[220:221], s[4:5], 0, v[132:133]
	global_load_lds_dwordx4 v[218:219], off
	s_mov_b32 m0, s40
	v_lshl_add_u64 v[234:235], s[4:5], 0, v[134:135]
	global_load_lds_dwordx4 v[220:221], off
	s_mov_b32 m0, s41
	s_nop 0
	global_load_lds_dwordx4 v[234:235], off
	s_waitcnt vmcnt(8)
	s_waitcnt lgkmcnt(0)
	s_barrier
	s_setprio 1
	s_waitcnt lgkmcnt(0)
	v_mfma_f32_16x16x32_bf16 v[62:65], v[144:147], v[176:179], v[62:65]
	v_mfma_f32_16x16x32_bf16 v[58:61], v[152:155], v[176:179], v[58:61]
	v_mfma_f32_16x16x32_bf16 v[46:49], v[144:147], v[184:187], v[46:49]
	v_mfma_f32_16x16x32_bf16 v[42:45], v[152:155], v[184:187], v[42:45]
	v_mfma_f32_16x16x32_bf16 v[30:33], v[144:147], v[192:195], v[30:33]
	v_mfma_f32_16x16x32_bf16 v[26:29], v[152:155], v[192:195], v[26:29]
	v_mfma_f32_16x16x32_bf16 v[14:17], v[144:147], v[206:209], v[14:17]
	v_mfma_f32_16x16x32_bf16 v[10:13], v[152:155], v[206:209], v[10:13]
	v_mfma_f32_16x16x32_bf16 v[62:65], v[148:151], v[180:183], v[62:65]
	v_mfma_f32_16x16x32_bf16 v[58:61], v[156:159], v[180:183], v[58:61]
	v_mfma_f32_16x16x32_bf16 v[46:49], v[148:151], v[188:191], v[46:49]
	v_mfma_f32_16x16x32_bf16 v[42:45], v[156:159], v[188:191], v[42:45]
	v_mfma_f32_16x16x32_bf16 v[30:33], v[148:151], v[202:205], v[30:33]
	v_mfma_f32_16x16x32_bf16 v[26:29], v[156:159], v[202:205], v[26:29]
	v_mfma_f32_16x16x32_bf16 v[14:17], v[148:151], v[210:213], v[14:17]
	v_mfma_f32_16x16x32_bf16 v[10:13], v[156:159], v[210:213], v[10:13]
	s_setprio 0
	s_setprio 1
	v_mfma_f32_16x16x32_bf16 v[54:57], v[160:163], v[176:179], v[54:57]
	v_mfma_f32_16x16x32_bf16 v[50:53], v[168:171], v[176:179], v[50:53]
	v_mfma_f32_16x16x32_bf16 v[38:41], v[160:163], v[184:187], v[38:41]
	v_mfma_f32_16x16x32_bf16 v[34:37], v[168:171], v[184:187], v[34:37]
	v_mfma_f32_16x16x32_bf16 v[22:25], v[160:163], v[192:195], v[22:25]
	v_mfma_f32_16x16x32_bf16 v[18:21], v[168:171], v[192:195], v[18:21]
	v_mfma_f32_16x16x32_bf16 v[6:9], v[160:163], v[206:209], v[6:9]
	v_mfma_f32_16x16x32_bf16 v[2:5], v[168:171], v[206:209], v[2:5]
	v_mfma_f32_16x16x32_bf16 v[54:57], v[164:167], v[180:183], v[54:57]
	v_mfma_f32_16x16x32_bf16 v[50:53], v[172:175], v[180:183], v[50:53]
	v_mfma_f32_16x16x32_bf16 v[38:41], v[164:167], v[188:191], v[38:41]
	v_mfma_f32_16x16x32_bf16 v[34:37], v[172:175], v[188:191], v[34:37]
	v_mfma_f32_16x16x32_bf16 v[22:25], v[164:167], v[202:205], v[22:25]
	v_mfma_f32_16x16x32_bf16 v[18:21], v[172:175], v[202:205], v[18:21]
	v_mfma_f32_16x16x32_bf16 v[6:9], v[164:167], v[210:213], v[6:9]
	v_mfma_f32_16x16x32_bf16 v[2:5], v[172:175], v[210:213], v[2:5]
	s_setprio 0
	s_barrier
	s_add_i32 s35, 0, 0x18000
	s_add_i32 s51, 0, 0x1c000
	v_add_u32_e32 v156, s35, v141
	v_add_u32_e32 v172, s51, v141
	ds_read_b128 v[144:147], v156
	ds_read_b128 v[148:151], v156 offset:1024
	ds_read_b128 v[152:155], v156 offset:2048
	ds_read_b128 v[156:159], v156 offset:3072
	ds_read_b128 v[160:163], v172
	ds_read_b128 v[164:167], v172 offset:1024
	ds_read_b128 v[168:171], v172 offset:2048
	ds_read_b128 v[172:175], v172 offset:3072
	s_add_u32 s4, s4, s8
	s_addc_u32 s5, s5, s9
	s_mov_b32 m0, s42
	v_lshl_add_u64 v[236:237], s[4:5], 0, v[132:133]
	ds_read_b128 v[176:179], v143 offset:32768
	ds_read_b128 v[180:183], v143 offset:33792
	ds_read_b128 v[184:187], v143 offset:34816
	ds_read_b128 v[188:191], v143 offset:35840
	ds_read_b128 v[192:195], v143 offset:36864
	ds_read_b128 v[202:205], v143 offset:37888
	ds_read_b128 v[206:209], v143 offset:38912
	ds_read_b128 v[210:213], v143 offset:39936
	global_load_lds_dwordx4 v[236:237], off
	v_lshl_add_u64 v[236:237], s[4:5], 0, v[134:135]
	s_mov_b32 m0, s43
	s_nop 0
	global_load_lds_dwordx4 v[236:237], off
	s_waitcnt vmcnt(8)
	s_waitcnt lgkmcnt(0)
	s_barrier
	s_setprio 1
	s_waitcnt lgkmcnt(0)
	v_mfma_f32_16x16x32_bf16 v[122:125], v[144:147], v[176:179], v[122:125]
	v_mfma_f32_16x16x32_bf16 v[126:129], v[152:155], v[176:179], v[126:129]
	v_mfma_f32_16x16x32_bf16 v[110:113], v[144:147], v[184:187], v[110:113]
	v_mfma_f32_16x16x32_bf16 v[106:109], v[152:155], v[184:187], v[106:109]
	v_mfma_f32_16x16x32_bf16 v[94:97], v[144:147], v[192:195], v[94:97]
	v_mfma_f32_16x16x32_bf16 v[90:93], v[152:155], v[192:195], v[90:93]
	v_mfma_f32_16x16x32_bf16 v[78:81], v[144:147], v[206:209], v[78:81]
	v_mfma_f32_16x16x32_bf16 v[74:77], v[152:155], v[206:209], v[74:77]
	v_mfma_f32_16x16x32_bf16 v[122:125], v[148:151], v[180:183], v[122:125]
	v_mfma_f32_16x16x32_bf16 v[126:129], v[156:159], v[180:183], v[126:129]
	v_mfma_f32_16x16x32_bf16 v[110:113], v[148:151], v[188:191], v[110:113]
	v_mfma_f32_16x16x32_bf16 v[106:109], v[156:159], v[188:191], v[106:109]
	v_mfma_f32_16x16x32_bf16 v[94:97], v[148:151], v[202:205], v[94:97]
	v_mfma_f32_16x16x32_bf16 v[90:93], v[156:159], v[202:205], v[90:93]
	v_mfma_f32_16x16x32_bf16 v[78:81], v[148:151], v[210:213], v[78:81]
	v_mfma_f32_16x16x32_bf16 v[74:77], v[156:159], v[210:213], v[74:77]
	s_setprio 0
	s_setprio 1
	v_mfma_f32_16x16x32_bf16 v[118:121], v[160:163], v[176:179], v[118:121]
	v_mfma_f32_16x16x32_bf16 v[114:117], v[168:171], v[176:179], v[114:117]
	v_mfma_f32_16x16x32_bf16 v[102:105], v[160:163], v[184:187], v[102:105]
	v_mfma_f32_16x16x32_bf16 v[98:101], v[168:171], v[184:187], v[98:101]
	v_mfma_f32_16x16x32_bf16 v[86:89], v[160:163], v[192:195], v[86:89]
	v_mfma_f32_16x16x32_bf16 v[82:85], v[168:171], v[192:195], v[82:85]
	v_mfma_f32_16x16x32_bf16 v[70:73], v[160:163], v[206:209], v[70:73]
	v_mfma_f32_16x16x32_bf16 v[66:69], v[168:171], v[206:209], v[66:69]
	v_mfma_f32_16x16x32_bf16 v[118:121], v[164:167], v[180:183], v[118:121]
	v_mfma_f32_16x16x32_bf16 v[114:117], v[172:175], v[180:183], v[114:117]
	v_mfma_f32_16x16x32_bf16 v[102:105], v[164:167], v[188:191], v[102:105]
	v_mfma_f32_16x16x32_bf16 v[98:101], v[172:175], v[188:191], v[98:101]
	v_mfma_f32_16x16x32_bf16 v[86:89], v[164:167], v[202:205], v[86:89]
	v_mfma_f32_16x16x32_bf16 v[82:85], v[172:175], v[202:205], v[82:85]
	v_mfma_f32_16x16x32_bf16 v[70:73], v[164:167], v[210:213], v[70:73]
	v_mfma_f32_16x16x32_bf16 v[66:69], v[172:175], v[210:213], v[66:69]
	s_setprio 0
	s_barrier
	s_add_i32 s4, s35, s39
	v_lshl_add_u64 v[196:197], v[196:197], 0, s[94:95]
	s_mov_b32 m0, s4
	ds_read_b128 v[176:179], v143 offset:49152
	ds_read_b128 v[180:183], v143 offset:50176
	ds_read_b128 v[184:187], v143 offset:51200
	ds_read_b128 v[188:191], v143 offset:52224
	ds_read_b128 v[192:195], v143 offset:53248
	ds_read_b128 v[202:205], v143 offset:54272
	ds_read_b128 v[206:209], v143 offset:55296
	ds_read_b128 v[210:213], v143 offset:56320
	global_load_lds_dwordx4 v[196:197], off
	v_lshl_add_u64 v[196:197], v[214:215], 0, s[94:95]
	s_add_i32 m0, s4, 0x2000
	s_add_i32 s4, s51, s39
	global_load_lds_dwordx4 v[196:197], off
	v_lshl_add_u64 v[196:197], v[216:217], 0, s[94:95]
	s_mov_b32 m0, s4
	s_nop 0
	global_load_lds_dwordx4 v[196:197], off
	v_lshl_add_u64 v[196:197], v[218:219], 0, s[94:95]
	s_add_i32 m0, s4, 0x2000
	s_nop 0
	global_load_lds_dwordx4 v[196:197], off
	v_lshl_add_u64 v[196:197], v[220:221], 0, s[94:95]
	s_mov_b32 m0, s45
	s_nop 0
	global_load_lds_dwordx4 v[196:197], off
	v_lshl_add_u64 v[196:197], v[234:235], 0, s[94:95]
	s_mov_b32 m0, s46
	s_nop 0
	global_load_lds_dwordx4 v[196:197], off
	s_waitcnt vmcnt(8)
	s_waitcnt lgkmcnt(0)
	s_barrier
	s_setprio 1
	s_waitcnt lgkmcnt(0)
	v_mfma_f32_16x16x32_bf16 v[62:65], v[144:147], v[176:179], v[62:65]
	v_mfma_f32_16x16x32_bf16 v[58:61], v[152:155], v[176:179], v[58:61]
	v_mfma_f32_16x16x32_bf16 v[46:49], v[144:147], v[184:187], v[46:49]
	v_mfma_f32_16x16x32_bf16 v[42:45], v[152:155], v[184:187], v[42:45]
	v_mfma_f32_16x16x32_bf16 v[30:33], v[144:147], v[192:195], v[30:33]
	v_mfma_f32_16x16x32_bf16 v[26:29], v[152:155], v[192:195], v[26:29]
	v_mfma_f32_16x16x32_bf16 v[14:17], v[144:147], v[206:209], v[14:17]
	v_mfma_f32_16x16x32_bf16 v[10:13], v[152:155], v[206:209], v[10:13]
	v_mfma_f32_16x16x32_bf16 v[62:65], v[148:151], v[180:183], v[62:65]
	v_mfma_f32_16x16x32_bf16 v[58:61], v[156:159], v[180:183], v[58:61]
	v_mfma_f32_16x16x32_bf16 v[46:49], v[148:151], v[188:191], v[46:49]
	v_mfma_f32_16x16x32_bf16 v[42:45], v[156:159], v[188:191], v[42:45]
	v_mfma_f32_16x16x32_bf16 v[30:33], v[148:151], v[202:205], v[30:33]
	v_mfma_f32_16x16x32_bf16 v[26:29], v[156:159], v[202:205], v[26:29]
	v_mfma_f32_16x16x32_bf16 v[14:17], v[148:151], v[210:213], v[14:17]
	v_mfma_f32_16x16x32_bf16 v[10:13], v[156:159], v[210:213], v[10:13]
	s_setprio 0
	s_setprio 1
	v_mfma_f32_16x16x32_bf16 v[54:57], v[160:163], v[176:179], v[54:57]
	v_mfma_f32_16x16x32_bf16 v[50:53], v[168:171], v[176:179], v[50:53]
	v_mfma_f32_16x16x32_bf16 v[38:41], v[160:163], v[184:187], v[38:41]
	v_mfma_f32_16x16x32_bf16 v[34:37], v[168:171], v[184:187], v[34:37]
	v_mfma_f32_16x16x32_bf16 v[22:25], v[160:163], v[192:195], v[22:25]
	v_mfma_f32_16x16x32_bf16 v[18:21], v[168:171], v[192:195], v[18:21]
	v_mfma_f32_16x16x32_bf16 v[6:9], v[160:163], v[206:209], v[6:9]
	v_mfma_f32_16x16x32_bf16 v[2:5], v[168:171], v[206:209], v[2:5]
	v_mfma_f32_16x16x32_bf16 v[54:57], v[164:167], v[180:183], v[54:57]
	v_mfma_f32_16x16x32_bf16 v[50:53], v[172:175], v[180:183], v[50:53]
	v_mfma_f32_16x16x32_bf16 v[38:41], v[164:167], v[188:191], v[38:41]
	v_mfma_f32_16x16x32_bf16 v[34:37], v[172:175], v[188:191], v[34:37]
	v_mfma_f32_16x16x32_bf16 v[22:25], v[164:167], v[202:205], v[22:25]
	v_mfma_f32_16x16x32_bf16 v[18:21], v[172:175], v[202:205], v[18:21]
	v_mfma_f32_16x16x32_bf16 v[6:9], v[164:167], v[210:213], v[6:9]
	v_mfma_f32_16x16x32_bf16 v[2:5], v[172:175], v[210:213], v[2:5]
	s_setprio 0
	s_barrier
	s_add_u32 s30, s30, 0x100
	s_addc_u32 s31, s31, 0
	s_add_u32 s19, s19, 0x100
	s_addc_u32 s21, s21, 0
	s_cmp_ge_i32 s34, s44
	s_mov_b32 s4, s34
	s_cbranch_scc0 .LBB0_544
.Lpeel_exit_2:
	v_readlane_b32 s56, v255, 52
	v_readlane_b32 s57, v255, 53
.LBB0_546:
	s_and_b64 vcc, exec, s[16:17]
	s_cbranch_vccz .LBB0_548
	s_barrier

.LBB0_838:
	s_andn2_b64 vcc, exec, s[14:15]
	s_cbranch_vccnz .LBB0_841
	s_add_u32 s24, s24, 0x80
	s_addc_u32 s25, s25, 0
	s_add_u32 s26, s26, 0x100
	s_addc_u32 s27, s27, 0
	s_mov_b32 s4, 0
	s_add_i32 s46, s4, 2
	s_add_u32 s47, s24, 0x80
	s_addc_u32 s5, s25, 0
	s_add_i32 s50, 0, 0x10000
	s_cmp_eq_u32 s41, s4
	s_cselect_b32 s5, s21, s5
	s_cselect_b32 s4, s20, s47
	v_add_u32_e32 v145, s50, v142
	s_cselect_b32 s49, s23, s27
	s_cselect_b32 s48, s22, s26
	s_add_i32 s47, 0, 0x14000
	ds_read_b128 v[146:149], v145
	ds_read_b128 v[150:153], v145 offset:1024
	ds_read_b128 v[154:157], v145 offset:2048
	ds_read_b128 v[158:161], v145 offset:3072
	v_add_u32_e32 v145, s47, v142
	ds_read_b128 v[162:165], v145
	ds_read_b128 v[166:169], v145 offset:1024
	ds_read_b128 v[170:173], v145 offset:2048
	ds_read_b128 v[174:177], v145 offset:3072
	v_lshl_add_u64 v[214:215], s[24:25], 0, v[136:137]
	s_add_i32 m0, s34, 0xc000
	ds_read_b128 v[178:181], v144
	ds_read_b128 v[182:185], v144 offset:1024
	ds_read_b128 v[186:189], v144 offset:2048
	ds_read_b128 v[190:193], v144 offset:3072
	ds_read_b128 v[194:197], v144 offset:4096
	ds_read_b128 v[202:205], v144 offset:5120
	ds_read_b128 v[206:209], v144 offset:6144
	ds_read_b128 v[210:213], v144 offset:7168
	global_load_lds_dwordx4 v[214:215], off
	v_lshl_add_u64 v[214:215], s[24:25], 0, v[138:139]
	s_add_i32 m0, s34, 0xe000
	s_nop 0
	global_load_lds_dwordx4 v[214:215], off
	s_waitcnt vmcnt(8)
	s_waitcnt lgkmcnt(0)
	s_barrier
	s_setprio 1
	s_waitcnt lgkmcnt(0)
	v_mfma_f32_16x16x32_bf16 v[126:129], v[146:149], v[178:181], 0
	v_mfma_f32_16x16x32_bf16 v[122:125], v[154:157], v[178:181], 0
	v_mfma_f32_16x16x32_bf16 v[110:113], v[146:149], v[186:189], 0
	v_mfma_f32_16x16x32_bf16 v[106:109], v[154:157], v[186:189], 0
	v_mfma_f32_16x16x32_bf16 v[94:97], v[146:149], v[194:197], 0
	v_mfma_f32_16x16x32_bf16 v[90:93], v[154:157], v[194:197], 0
	v_mfma_f32_16x16x32_bf16 v[78:81], v[146:149], v[206:209], 0
	v_mfma_f32_16x16x32_bf16 v[74:77], v[154:157], v[206:209], 0
	v_mfma_f32_16x16x32_bf16 v[126:129], v[150:153], v[182:185], v[126:129]
	v_mfma_f32_16x16x32_bf16 v[122:125], v[158:161], v[182:185], v[122:125]
	v_mfma_f32_16x16x32_bf16 v[110:113], v[150:153], v[190:193], v[110:113]
	v_mfma_f32_16x16x32_bf16 v[106:109], v[158:161], v[190:193], v[106:109]
	v_mfma_f32_16x16x32_bf16 v[94:97], v[150:153], v[202:205], v[94:97]
	v_mfma_f32_16x16x32_bf16 v[90:93], v[158:161], v[202:205], v[90:93]
	v_mfma_f32_16x16x32_bf16 v[78:81], v[150:153], v[210:213], v[78:81]
	v_mfma_f32_16x16x32_bf16 v[74:77], v[158:161], v[210:213], v[74:77]
	s_setprio 0
	s_setprio 1
	v_mfma_f32_16x16x32_bf16 v[118:121], v[162:165], v[178:181], 0
	v_mfma_f32_16x16x32_bf16 v[114:117], v[170:173], v[178:181], 0
	v_mfma_f32_16x16x32_bf16 v[102:105], v[162:165], v[186:189], 0
	v_mfma_f32_16x16x32_bf16 v[98:101], v[170:173], v[186:189], 0
	v_mfma_f32_16x16x32_bf16 v[86:89], v[162:165], v[194:197], 0
	v_mfma_f32_16x16x32_bf16 v[82:85], v[170:173], v[194:197], 0
	v_mfma_f32_16x16x32_bf16 v[70:73], v[162:165], v[206:209], 0
	v_mfma_f32_16x16x32_bf16 v[66:69], v[170:173], v[206:209], 0
	v_mfma_f32_16x16x32_bf16 v[118:121], v[166:169], v[182:185], v[118:121]
	v_mfma_f32_16x16x32_bf16 v[114:117], v[174:177], v[182:185], v[114:117]
	v_mfma_f32_16x16x32_bf16 v[102:105], v[166:169], v[190:193], v[102:105]
	v_mfma_f32_16x16x32_bf16 v[98:101], v[174:177], v[190:193], v[98:101]
	v_mfma_f32_16x16x32_bf16 v[86:89], v[166:169], v[202:205], v[86:89]
	v_mfma_f32_16x16x32_bf16 v[82:85], v[174:177], v[202:205], v[82:85]
	v_mfma_f32_16x16x32_bf16 v[70:73], v[166:169], v[210:213], v[70:73]
	v_mfma_f32_16x16x32_bf16 v[66:69], v[174:177], v[210:213], v[66:69]
	s_setprio 0
	s_barrier
	s_add_i32 s50, s50, s31
	v_lshl_add_u64 v[214:215], s[48:49], 0, v[0:1]
	s_mov_b32 m0, s50
	ds_read_b128 v[178:181], v144 offset:16384
	ds_read_b128 v[182:185], v144 offset:17408
	ds_read_b128 v[186:189], v144 offset:18432
	ds_read_b128 v[190:193], v144 offset:19456
	ds_read_b128 v[194:197], v144 offset:20480
	ds_read_b128 v[202:205], v144 offset:21504
	ds_read_b128 v[206:209], v144 offset:22528
	ds_read_b128 v[210:213], v144 offset:23552
	global_load_lds_dwordx4 v[214:215], off
	s_add_i32 m0, s50, 0x2000
	v_lshl_add_u64 v[216:217], s[48:49], 0, v[130:131]
	s_add_u32 s48, s48, s8
	s_addc_u32 s49, s49, s9
	s_add_i32 s47, s47, s31
	global_load_lds_dwordx4 v[216:217], off
	v_lshl_add_u64 v[218:219], s[48:49], 0, v[0:1]
	s_mov_b32 m0, s47
	v_lshl_add_u64 v[220:221], s[48:49], 0, v[130:131]
	global_load_lds_dwordx4 v[218:219], off
	s_add_i32 m0, s47, 0x2000
	v_lshl_add_u64 v[234:235], s[4:5], 0, v[132:133]
	global_load_lds_dwordx4 v[220:221], off
	s_mov_b32 m0, s34
	v_lshl_add_u64 v[236:237], s[4:5], 0, v[134:135]
	global_load_lds_dwordx4 v[234:235], off
	s_mov_b32 m0, s35
	s_nop 0
	global_load_lds_dwordx4 v[236:237], off
	s_waitcnt vmcnt(8)
	s_waitcnt lgkmcnt(0)
	s_barrier
	s_setprio 1
	s_waitcnt lgkmcnt(0)
	v_mfma_f32_16x16x32_bf16 v[62:65], v[146:149], v[178:181], 0
	v_mfma_f32_16x16x32_bf16 v[58:61], v[154:157], v[178:181], 0
	v_mfma_f32_16x16x32_bf16 v[46:49], v[146:149], v[186:189], 0
	v_mfma_f32_16x16x32_bf16 v[42:45], v[154:157], v[186:189], 0
	v_mfma_f32_16x16x32_bf16 v[30:33], v[146:149], v[194:197], 0
	v_mfma_f32_16x16x32_bf16 v[26:29], v[154:157], v[194:197], 0
	v_mfma_f32_16x16x32_bf16 v[14:17], v[146:149], v[206:209], 0
	v_mfma_f32_16x16x32_bf16 v[10:13], v[154:157], v[206:209], 0
	v_mfma_f32_16x16x32_bf16 v[62:65], v[150:153], v[182:185], v[62:65]
	v_mfma_f32_16x16x32_bf16 v[58:61], v[158:161], v[182:185], v[58:61]
	v_mfma_f32_16x16x32_bf16 v[46:49], v[150:153], v[190:193], v[46:49]
	v_mfma_f32_16x16x32_bf16 v[42:45], v[158:161], v[190:193], v[42:45]
	v_mfma_f32_16x16x32_bf16 v[30:33], v[150:153], v[202:205], v[30:33]
	v_mfma_f32_16x16x32_bf16 v[26:29], v[158:161], v[202:205], v[26:29]
	v_mfma_f32_16x16x32_bf16 v[14:17], v[150:153], v[210:213], v[14:17]
	v_mfma_f32_16x16x32_bf16 v[10:13], v[158:161], v[210:213], v[10:13]
	s_setprio 0
	s_setprio 1
	v_mfma_f32_16x16x32_bf16 v[54:57], v[162:165], v[178:181], 0
	v_mfma_f32_16x16x32_bf16 v[50:53], v[170:173], v[178:181], 0
	v_mfma_f32_16x16x32_bf16 v[38:41], v[162:165], v[186:189], 0
	v_mfma_f32_16x16x32_bf16 v[34:37], v[170:173], v[186:189], 0
	v_mfma_f32_16x16x32_bf16 v[22:25], v[162:165], v[194:197], 0
	v_mfma_f32_16x16x32_bf16 v[18:21], v[170:173], v[194:197], 0
	v_mfma_f32_16x16x32_bf16 v[6:9], v[162:165], v[206:209], 0
	v_mfma_f32_16x16x32_bf16 v[2:5], v[170:173], v[206:209], 0
	v_mfma_f32_16x16x32_bf16 v[54:57], v[166:169], v[182:185], v[54:57]
	v_mfma_f32_16x16x32_bf16 v[50:53], v[174:177], v[182:185], v[50:53]
	v_mfma_f32_16x16x32_bf16 v[38:41], v[166:169], v[190:193], v[38:41]
	v_mfma_f32_16x16x32_bf16 v[34:37], v[174:177], v[190:193], v[34:37]
	v_mfma_f32_16x16x32_bf16 v[22:25], v[166:169], v[202:205], v[22:25]
	v_mfma_f32_16x16x32_bf16 v[18:21], v[174:177], v[202:205], v[18:21]
	v_mfma_f32_16x16x32_bf16 v[6:9], v[166:169], v[210:213], v[6:9]
	v_mfma_f32_16x16x32_bf16 v[2:5], v[174:177], v[210:213], v[2:5]
	s_setprio 0
	s_barrier
	s_add_i32 s47, 0, 0x18000
	v_add_u32_e32 v145, s47, v142
	s_add_i32 s48, 0, 0x1c000
	ds_read_b128 v[146:149], v145
	ds_read_b128 v[150:153], v145 offset:1024
	ds_read_b128 v[154:157], v145 offset:2048
	ds_read_b128 v[158:161], v145 offset:3072
	v_add_u32_e32 v145, s48, v142
	ds_read_b128 v[162:165], v145
	ds_read_b128 v[166:169], v145 offset:1024
	ds_read_b128 v[170:173], v145 offset:2048
	ds_read_b128 v[174:177], v145 offset:3072
	s_add_u32 s4, s4, s8
	s_addc_u32 s5, s5, s9
	s_mov_b32 m0, s36
	v_lshl_add_u64 v[238:239], s[4:5], 0, v[132:133]
	ds_read_b128 v[178:181], v144 offset:32768
	ds_read_b128 v[182:185], v144 offset:33792
	ds_read_b128 v[186:189], v144 offset:34816
	ds_read_b128 v[190:193], v144 offset:35840
	ds_read_b128 v[194:197], v144 offset:36864
	ds_read_b128 v[202:205], v144 offset:37888
	ds_read_b128 v[206:209], v144 offset:38912
	ds_read_b128 v[210:213], v144 offset:39936
	global_load_lds_dwordx4 v[238:239], off
	v_lshl_add_u64 v[238:239], s[4:5], 0, v[134:135]
	s_mov_b32 m0, s37
	s_nop 0
	global_load_lds_dwordx4 v[238:239], off
	s_waitcnt vmcnt(8)
	s_waitcnt lgkmcnt(0)
	s_barrier
	s_setprio 1
	s_waitcnt lgkmcnt(0)
	v_mfma_f32_16x16x32_bf16 v[126:129], v[146:149], v[178:181], v[126:129]
	v_mfma_f32_16x16x32_bf16 v[122:125], v[154:157], v[178:181], v[122:125]
	v_mfma_f32_16x16x32_bf16 v[110:113], v[146:149], v[186:189], v[110:113]
	v_mfma_f32_16x16x32_bf16 v[106:109], v[154:157], v[186:189], v[106:109]
	v_mfma_f32_16x16x32_bf16 v[94:97], v[146:149], v[194:197], v[94:97]
	v_mfma_f32_16x16x32_bf16 v[90:93], v[154:157], v[194:197], v[90:93]
	v_mfma_f32_16x16x32_bf16 v[78:81], v[146:149], v[206:209], v[78:81]
	v_mfma_f32_16x16x32_bf16 v[74:77], v[154:157], v[206:209], v[74:77]
	v_mfma_f32_16x16x32_bf16 v[126:129], v[150:153], v[182:185], v[126:129]
	v_mfma_f32_16x16x32_bf16 v[122:125], v[158:161], v[182:185], v[122:125]
	v_mfma_f32_16x16x32_bf16 v[110:113], v[150:153], v[190:193], v[110:113]
	v_mfma_f32_16x16x32_bf16 v[106:109], v[158:161], v[190:193], v[106:109]
	v_mfma_f32_16x16x32_bf16 v[94:97], v[150:153], v[202:205], v[94:97]
	v_mfma_f32_16x16x32_bf16 v[90:93], v[158:161], v[202:205], v[90:93]
	v_mfma_f32_16x16x32_bf16 v[78:81], v[150:153], v[210:213], v[78:81]
	v_mfma_f32_16x16x32_bf16 v[74:77], v[158:161], v[210:213], v[74:77]
	s_setprio 0
	s_setprio 1
	v_mfma_f32_16x16x32_bf16 v[118:121], v[162:165], v[178:181], v[118:121]
	v_mfma_f32_16x16x32_bf16 v[114:117], v[170:173], v[178:181], v[114:117]
	v_mfma_f32_16x16x32_bf16 v[102:105], v[162:165], v[186:189], v[102:105]
	v_mfma_f32_16x16x32_bf16 v[98:101], v[170:173], v[186:189], v[98:101]
	v_mfma_f32_16x16x32_bf16 v[86:89], v[162:165], v[194:197], v[86:89]
	v_mfma_f32_16x16x32_bf16 v[82:85], v[170:173], v[194:197], v[82:85]
	v_mfma_f32_16x16x32_bf16 v[70:73], v[162:165], v[206:209], v[70:73]
	v_mfma_f32_16x16x32_bf16 v[66:69], v[170:173], v[206:209], v[66:69]
	v_mfma_f32_16x16x32_bf16 v[118:121], v[166:169], v[182:185], v[118:121]
	v_mfma_f32_16x16x32_bf16 v[114:117], v[174:177], v[182:185], v[114:117]
	v_mfma_f32_16x16x32_bf16 v[102:105], v[166:169], v[190:193], v[102:105]
	v_mfma_f32_16x16x32_bf16 v[98:101], v[174:177], v[190:193], v[98:101]
	v_mfma_f32_16x16x32_bf16 v[86:89], v[166:169], v[202:205], v[86:89]
	v_mfma_f32_16x16x32_bf16 v[82:85], v[174:177], v[202:205], v[82:85]
	v_mfma_f32_16x16x32_bf16 v[70:73], v[166:169], v[210:213], v[70:73]
	v_mfma_f32_16x16x32_bf16 v[66:69], v[174:177], v[210:213], v[66:69]
	s_setprio 0
	s_barrier
	s_add_i32 s4, s47, s31
	v_lshl_add_u64 v[214:215], v[214:215], 0, s[94:95]
	s_mov_b32 m0, s4
	ds_read_b128 v[178:181], v144 offset:49152
	ds_read_b128 v[182:185], v144 offset:50176
	ds_read_b128 v[186:189], v144 offset:51200
	ds_read_b128 v[190:193], v144 offset:52224
	ds_read_b128 v[194:197], v144 offset:53248
	ds_read_b128 v[202:205], v144 offset:54272
	ds_read_b128 v[206:209], v144 offset:55296
	ds_read_b128 v[210:213], v144 offset:56320
	global_load_lds_dwordx4 v[214:215], off
	v_lshl_add_u64 v[214:215], v[216:217], 0, s[94:95]
	s_add_i32 m0, s4, 0x2000
	s_add_i32 s4, s48, s31
	global_load_lds_dwordx4 v[214:215], off
	v_lshl_add_u64 v[214:215], v[218:219], 0, s[94:95]
	s_mov_b32 m0, s4
	s_nop 0
	global_load_lds_dwordx4 v[214:215], off
	v_lshl_add_u64 v[214:215], v[220:221], 0, s[94:95]
	s_add_i32 m0, s4, 0x2000
	s_nop 0
	global_load_lds_dwordx4 v[214:215], off
	v_lshl_add_u64 v[214:215], v[234:235], 0, s[94:95]
	s_mov_b32 m0, s39
	s_nop 0
	global_load_lds_dwordx4 v[214:215], off
	v_lshl_add_u64 v[214:215], v[236:237], 0, s[94:95]
	s_mov_b32 m0, s40
	s_nop 0
	global_load_lds_dwordx4 v[214:215], off
	s_waitcnt vmcnt(8)
	s_waitcnt lgkmcnt(0)
	s_barrier
	s_setprio 1
	s_waitcnt lgkmcnt(0)
	v_mfma_f32_16x16x32_bf16 v[62:65], v[146:149], v[178:181], v[62:65]
	v_mfma_f32_16x16x32_bf16 v[58:61], v[154:157], v[178:181], v[58:61]
	v_mfma_f32_16x16x32_bf16 v[46:49], v[146:149], v[186:189], v[46:49]
	v_mfma_f32_16x16x32_bf16 v[42:45], v[154:157], v[186:189], v[42:45]
	v_mfma_f32_16x16x32_bf16 v[30:33], v[146:149], v[194:197], v[30:33]
	v_mfma_f32_16x16x32_bf16 v[26:29], v[154:157], v[194:197], v[26:29]
	v_mfma_f32_16x16x32_bf16 v[14:17], v[146:149], v[206:209], v[14:17]
	v_mfma_f32_16x16x32_bf16 v[10:13], v[154:157], v[206:209], v[10:13]
	v_mfma_f32_16x16x32_bf16 v[62:65], v[150:153], v[182:185], v[62:65]
	v_mfma_f32_16x16x32_bf16 v[58:61], v[158:161], v[182:185], v[58:61]
	v_mfma_f32_16x16x32_bf16 v[46:49], v[150:153], v[190:193], v[46:49]
	v_mfma_f32_16x16x32_bf16 v[42:45], v[158:161], v[190:193], v[42:45]
	v_mfma_f32_16x16x32_bf16 v[30:33], v[150:153], v[202:205], v[30:33]
	v_mfma_f32_16x16x32_bf16 v[26:29], v[158:161], v[202:205], v[26:29]
	v_mfma_f32_16x16x32_bf16 v[14:17], v[150:153], v[210:213], v[14:17]
	v_mfma_f32_16x16x32_bf16 v[10:13], v[158:161], v[210:213], v[10:13]
	s_setprio 0
	s_setprio 1
	v_mfma_f32_16x16x32_bf16 v[54:57], v[162:165], v[178:181], v[54:57]
	v_mfma_f32_16x16x32_bf16 v[50:53], v[170:173], v[178:181], v[50:53]
	v_mfma_f32_16x16x32_bf16 v[38:41], v[162:165], v[186:189], v[38:41]
	v_mfma_f32_16x16x32_bf16 v[34:37], v[170:173], v[186:189], v[34:37]
	v_mfma_f32_16x16x32_bf16 v[22:25], v[162:165], v[194:197], v[22:25]
	v_mfma_f32_16x16x32_bf16 v[18:21], v[170:173], v[194:197], v[18:21]
	v_mfma_f32_16x16x32_bf16 v[6:9], v[162:165], v[206:209], v[6:9]
	v_mfma_f32_16x16x32_bf16 v[2:5], v[170:173], v[206:209], v[2:5]
	v_mfma_f32_16x16x32_bf16 v[54:57], v[166:169], v[182:185], v[54:57]
	v_mfma_f32_16x16x32_bf16 v[50:53], v[174:177], v[182:185], v[50:53]
	v_mfma_f32_16x16x32_bf16 v[38:41], v[166:169], v[190:193], v[38:41]
	v_mfma_f32_16x16x32_bf16 v[34:37], v[174:177], v[190:193], v[34:37]
	v_mfma_f32_16x16x32_bf16 v[22:25], v[166:169], v[202:205], v[22:25]
	v_mfma_f32_16x16x32_bf16 v[18:21], v[174:177], v[202:205], v[18:21]
	v_mfma_f32_16x16x32_bf16 v[6:9], v[166:169], v[210:213], v[6:9]
	v_mfma_f32_16x16x32_bf16 v[2:5], v[174:177], v[210:213], v[2:5]
	s_setprio 0
	s_barrier
	s_add_u32 s24, s24, 0x100
	s_addc_u32 s25, s25, 0
	s_add_u32 s26, s26, 0x100
	s_addc_u32 s27, s27, 0
	s_cmp_ge_i32 s46, s38
	s_mov_b32 s4, s46
	s_cbranch_scc1 .LBB0_841

.LBB0_990:
	s_mul_hi_u32 s6, s30, s26
	s_mul_i32 s6, s6, s33
	s_sub_i32 s6, s30, s6
	s_sub_i32 s7, s6, s33
	s_cmp_ge_u32 s6, s33
	s_cselect_b32 s6, s7, s6
	s_sub_i32 s7, s6, s33
	s_cmp_ge_u32 s6, s33
	s_cselect_b32 s6, s7, s6
	s_sub_i32 s6, s19, s6
	s_mul_hi_u32 s7, s6, s26
	s_mul_i32 s7, s7, s33
	s_sub_i32 s6, s6, s7
	s_sub_i32 s7, s6, s33
	s_cmp_ge_u32 s6, s33
	s_cselect_b32 s6, s7, s6
	s_sub_i32 s7, s6, s33
	s_cmp_ge_u32 s6, s33
	s_cselect_b32 s6, s7, s6
	s_cmp_eq_u32 s16, 1
	s_cbranch_scc1 .LBB0_993
	s_cmpk_gt_i32 s6, 0x2eff
	s_cbranch_scc1 .LBB0_993
	s_mul_i32 s7, s16, 0x2f00000
	s_add_u32 s7, s3, s7
	s_mul_i32 s10, s16, 0x5e00000
	s_mov_b32 s11, s17
	s_addc_u32 s8, s18, 0
	v_lshl_add_u64 v[24:25], v[6:7], 0, s[10:11]
	s_lshl_b32 s9, s6, 5
